# W10 + in-proj epilogue specialised per column-tile mode (rotary / silu / plain): three straight-line copies with the uniform mode branches resolved, dead cos/sin constant moves and acc->temp moves rem
# speedup vs baseline: 1.0049x; 1.0049x over previous
.LBB0_314:
	s_mov_b32 s0, -1
	v_mov_b32_e32 v195, 4
	v_mbcnt_lo_u32_b32 v40, s0, 0
	v_mbcnt_hi_u32_b32 v41, s0, v40
	s_lshl_b32 s0, s22, 8
	v_lshrrev_b32_e32 v40, 4, v41
	s_or_b32 s0, s0, s85
	v_lshl_add_u32 v193, v40, 3, s0
	s_movk_i32 s0, 0xc00
	v_mul_hi_i32 v42, v193, s6
	v_cmp_gt_i32_e64 s[42:43], s0, v193
	v_add_u32_e32 v203, 0xfffff400, v193
	v_mov_b32_e32 v196, 0x3000000
	v_lshrrev_b32_e32 v201, 31, v42
	v_lshrrev_b32_e32 v204, 7, v42
	v_mov_b32_e32 v200, 0x3000000
	v_mov_b32_e32 v202, 4
	s_and_saveexec_b64 s[0:1], s[42:43]
	v_add_u32_e32 v42, v204, v201
	s_mov_b32 s4, 0xc00000
	v_mul_lo_u32 v200, v42, s4
	v_mov_b32_e32 v202, 6
	v_mov_b32_e32 v203, v193
	s_or_b64 exec, exec, s[0:1]
	v_add_u32_e32 v194, 0x80, v193
	s_movk_i32 s0, 0xb80
	v_mul_hi_i32 v42, v194, s6
	v_cmp_gt_i32_e64 s[44:45], s0, v193
	v_add_u32_e32 v199, 0xfffff480, v193
	v_lshrrev_b32_e32 v197, 31, v42
	v_lshrrev_b32_e32 v198, 7, v42
	s_and_saveexec_b64 s[0:1], s[44:45]
	v_add_u32_e32 v42, v198, v197
	s_mov_b32 s4, 0xc00000
	v_mul_lo_u32 v196, v42, s4
	v_mov_b32_e32 v195, 6
	v_mov_b32_e32 v199, v194
	s_or_b64 exec, exec, s[0:1]
	s_lshl_b32 s8, s2, 8
	s_add_i32 s8, s8, s84
	s_cmp_lt_i32 s22, 6
	s_cselect_b64 s[80:81], -1, 0
	s_add_i32 s0, s22, -9
	s_sub_i32 s1, s22, 20
	s_min_u32 s0, s0, s1
	s_cmp_lt_u32 s0, 3
	v_and_b32_e32 v192, 15, v41
	s_cselect_b64 s[0:1], -1, 0
	s_and_b64 vcc, exec, s[80:81]
	s_cbranch_vccnz .Lepiz_m1
	s_and_b64 vcc, exec, s[0:1]
	s_cbranch_vccnz .Lepiz_m2
	v_cndmask_b32_e64 v172, 0, 1, s[80:81]
	v_cmp_ne_u32_e64 s[40:41], 1, v172
	s_waitcnt vmcnt(0)
	s_mov_b64 s[4:5], -1
	v_cndmask_b32_e64 v159, 0, 1, s[0:1]
	v_cmp_ne_u32_e64 s[38:39], 1, v159
	v_mov_b32_e32 v156, v148
	v_mov_b32_e32 v179, v149
	v_mov_b32_e32 v180, v150
	v_mov_b32_e32 v182, v151
	v_mov_b32_e32 v178, v144
	v_mov_b32_e32 v185, v145
	v_mov_b32_e32 v186, v146
	v_mov_b32_e32 v188, v147
	s_lshr_b32 s0, s8, 4
	s_and_b32 s4, s0, 0xfc
	s_ashr_i32 s0, s2, 31
	s_lshr_b32 s0, s0, 28
	s_add_i32 s0, s2, s0
	s_ashr_i32 s13, s0, 4
	v_add_u32_e32 v144, v204, v201
	s_movk_i32 s0, 0x300
	v_mul_lo_u32 v144, v144, s0
	v_sub_u32_e32 v144, v193, v144
	v_cndmask_b32_e64 v146, v203, v144, s[42:43]
	v_lshrrev_b32_e32 v144, 7, v146
	v_mad_u64_u32 v[144:145], s[0:1], v202, s13, v[144:145]
	v_lshlrev_b32_e32 v145, 4, v146
	v_lshl_add_u32 v144, v144, 19, v200
	v_and_b32_e32 v145, 0x600, v145
	v_and_b32_e32 v146, 31, v146
	v_or3_b32 v146, v144, v145, v146
	v_add_u32_e32 v144, 0xfffff200, v193
	v_mul_hi_i32 v145, v144, s6
	v_lshrrev_b32_e32 v147, 31, v145
	v_ashrrev_i32_e32 v145, 6, v145
	v_add_u32_e32 v145, v145, v147
	v_mul_i32_i24_e32 v147, 0x180, v145
	v_sub_u32_e32 v144, v144, v147
	v_mul_i32_i24_e32 v147, 0x2aab, v144
	v_mov_b32_e32 v148, 4
	v_ashrrev_i16_sdwa v148, v148, v147 dst_sel:DWORD dst_unused:UNUSED_PAD src0_sel:DWORD src1_sel:WORD_1
	v_lshrrev_b32_e32 v147, 31, v147
	v_add_u16_e32 v147, v148, v147
	v_mul_lo_u16_e32 v148, 0x60, v147
	v_sub_u16_e32 v144, v144, v148
	s_lshl_b32 s5, s13, 2
	v_bfe_i32 v148, v144, 0, 16
	v_mul_i32_i24_e32 v144, 0x600000, v145
	v_and_or_b32 v144, v148, 31, v144
	v_add_u32_e32 v145, s5, v147
	s_mov_b32 s0, 0x60000
	v_lshlrev_b32_e32 v147, 4, v148
	v_mad_u64_u32 v[144:145], s[0:1], v145, s0, v[144:145]
	v_and_b32_e32 v147, 0xfffffe00, v147
	s_mov_b32 s0, 0x3800000
	v_add3_u32 v147, v144, v147, s0
	v_add_u32_e32 v144, 0xffffef00, v193
	v_mul_hi_i32 v145, v144, s6
	v_lshrrev_b32_e32 v148, 31, v145
	v_ashrrev_i32_e32 v145, 7, v145
	v_add_u32_e32 v145, v145, v148
	v_mul_i32_i24_e32 v148, 0x300, v145
	v_sub_u32_e32 v144, v144, v148
	v_mul_i32_i24_e32 v148, 0x2aab, v144
	v_mov_b32_e32 v149, 5
	v_ashrrev_i16_sdwa v149, v149, v148 dst_sel:DWORD dst_unused:UNUSED_PAD src0_sel:DWORD src1_sel:WORD_1
	v_lshrrev_b32_e32 v148, 31, v148
	v_add_u16_e32 v148, v149, v148
	v_mul_lo_u16_e32 v149, 0xc0, v148
	v_sub_u16_e32 v144, v144, v149
	s_mov_b32 s0, 0xc00000
	v_bfe_i32 v149, v144, 0, 16
	v_mul_lo_u32 v144, v145, s0
	v_and_or_b32 v144, v149, 31, v144
	v_add_u32_e32 v145, s5, v148
	s_mov_b32 s0, 0xc0000
	v_lshlrev_b32_e32 v148, 4, v149
	v_mad_u64_u32 v[144:145], s[0:1], v145, s0, v[144:145]
	v_and_b32_e32 v148, 0xfffffe00, v148
	s_mov_b32 s0, 0x4400000
	v_add3_u32 v144, v144, v148, s0
	s_movk_i32 s0, 0xe00
	s_lshl_b32 s2, s13, 16
	v_cmp_gt_i32_e32 vcc, s0, v193
	s_movk_i32 s0, 0x1710
	s_add_i32 s2, s2, 0x5bfe900
	v_cmp_gt_u32_e64 s[42:43], s0, v193
	s_movk_i32 s0, 0x1700
	v_add_u32_e32 v145, s2, v193
	v_cndmask_b32_e64 v149, 0, v237, s[42:43]
	v_cmp_gt_i32_e64 s[46:47], s0, v193
	s_movk_i32 s0, 0x1100
	v_cndmask_b32_e32 v148, v236, v218, vcc
	v_cndmask_b32_e64 v149, v149, v239, s[46:47]
	v_cmp_gt_i32_e64 s[42:43], s0, v193
	v_cndmask_b32_e64 v144, v145, v144, s[46:47]
	s_nop 0
	v_cndmask_b32_e64 v159, v149, v148, s[42:43]
	v_cndmask_b32_e64 v144, v144, v147, s[42:43]
	v_cndmask_b32_e32 v181, v144, v146, vcc
	v_cvt_pk_bf16_f32 v144, v156, v179
	v_cvt_pk_bf16_f32 v145, v180, v182
	v_cmp_ne_u32_e64 s[42:43], 0, v159
	v_cndmask_b32_e64 v180, 4, 5, s[46:47]
	v_cvt_pk_bf16_f32 v146, v178, v185
	v_cvt_pk_bf16_f32 v147, v186, v188
	s_and_saveexec_b64 s[0:1], s[42:43]
	v_mul_u32_u24_e32 v148, s4, v159
	v_lshl_or_b32 v148, v192, v180, v148
	v_add_u32_e32 v212, v148, v181
	v_lshl_add_u64 v[148:149], v[212:213], 1, s[52:53]
	global_store_dwordx4 v[148:149], v[144:147], off nt
	s_nop 1
	s_or_b64 exec, exec, s[0:1]
	s_mov_b64 s[0:1], -1
	v_mov_b32_e32 v144, v136
	v_mov_b32_e32 v145, v137
	v_mov_b32_e32 v146, v138
	v_mov_b32_e32 v148, v139
	v_mov_b32_e32 v147, v132
	v_mov_b32_e32 v151, v133
	v_mov_b32_e32 v178, v134
	v_mov_b32_e32 v156, v135
	v_add_u32_e32 v132, v198, v197
	s_movk_i32 s0, 0x300
	v_mul_lo_u32 v132, v132, s0
	v_sub_u32_e32 v132, v194, v132
	v_cndmask_b32_e64 v134, v199, v132, s[44:45]
	v_lshrrev_b32_e32 v132, 7, v134
	v_mad_u64_u32 v[132:133], s[0:1], v195, s13, v[132:133]
	v_lshlrev_b32_e32 v133, 4, v134
	v_lshl_add_u32 v132, v132, 19, v196
	v_and_b32_e32 v133, 0x600, v133
	v_and_b32_e32 v134, 31, v134
	v_or3_b32 v134, v132, v133, v134
	v_add_u32_e32 v132, 0xfffff280, v193
	v_mul_hi_i32 v133, v132, s6
	v_lshrrev_b32_e32 v135, 31, v133
	v_ashrrev_i32_e32 v133, 6, v133
	v_add_u32_e32 v133, v133, v135
	v_mul_i32_i24_e32 v135, 0x180, v133
	v_sub_u32_e32 v132, v132, v135
	v_mul_i32_i24_e32 v135, 0x2aab, v132
	v_lshrrev_b32_e32 v136, 31, v135
	v_ashrrev_i32_e32 v135, 20, v135
	v_add_u16_e32 v135, v135, v136
	v_mul_lo_u16_e32 v136, 0x60, v135
	v_sub_u16_e32 v132, v132, v136
	v_bfe_i32 v136, v132, 0, 16
	v_mul_i32_i24_e32 v132, 0x600000, v133
	v_and_or_b32 v132, v136, 31, v132
	v_add_u32_e32 v133, s5, v135
	s_mov_b32 s0, 0x60000
	v_lshlrev_b32_e32 v135, 4, v136
	v_mad_u64_u32 v[132:133], s[0:1], v133, s0, v[132:133]
	v_and_b32_e32 v135, 0xfffffe00, v135
	s_mov_b32 s0, 0x3800000
	v_add3_u32 v135, v132, v135, s0
	v_add_u32_e32 v132, 0xffffef80, v193
	v_mul_hi_i32 v133, v132, s6
	v_lshrrev_b32_e32 v136, 31, v133
	v_ashrrev_i32_e32 v133, 7, v133
	v_add_u32_e32 v133, v133, v136
	v_mul_i32_i24_e32 v136, 0x300, v133
	v_sub_u32_e32 v132, v132, v136
	v_mul_i32_i24_e32 v136, 0x2aab, v132
	v_lshrrev_b32_e32 v137, 31, v136
	v_ashrrev_i32_e32 v136, 21, v136
	v_add_u16_e32 v136, v136, v137
	v_mul_lo_u16_e32 v137, 0xc0, v136
	v_sub_u16_e32 v132, v132, v137
	s_mov_b32 s0, 0xc00000
	v_bfe_i32 v137, v132, 0, 16
	v_mul_lo_u32 v132, v133, s0
	v_and_or_b32 v132, v137, 31, v132
	v_add_u32_e32 v133, s5, v136
	s_mov_b32 s0, 0xc0000
	v_lshlrev_b32_e32 v136, 4, v137
	v_mad_u64_u32 v[132:133], s[0:1], v133, s0, v[132:133]
	v_and_b32_e32 v136, 0xfffffe00, v136
	s_mov_b32 s0, 0x4400000
	v_add3_u32 v132, v132, v136, s0
	s_movk_i32 s0, 0xd80
	v_cmp_gt_i32_e32 vcc, s0, v193
	s_movk_i32 s0, 0x1710
	v_cmp_gt_u32_e64 s[44:45], s0, v194
	s_movk_i32 s0, 0x1680
	v_add_u32_e32 v133, s2, v194
	v_cndmask_b32_e64 v137, 0, v237, s[44:45]
	v_cmp_gt_i32_e64 s[46:47], s0, v193
	s_movk_i32 s0, 0x1080
	v_cndmask_b32_e32 v136, v236, v218, vcc
	v_cndmask_b32_e64 v137, v137, v239, s[46:47]
	v_cmp_gt_i32_e64 s[44:45], s0, v193
	v_cndmask_b32_e64 v132, v133, v132, s[46:47]
	s_nop 0
	v_cndmask_b32_e64 v158, v137, v136, s[44:45]
	v_cndmask_b32_e64 v132, v132, v135, s[44:45]
	v_cndmask_b32_e32 v172, v132, v134, vcc
	v_cvt_pk_bf16_f32 v132, v144, v145
	v_cmp_ne_u32_e64 s[44:45], 0, v158
	v_cndmask_b32_e64 v145, 4, 5, s[46:47]
	v_cvt_pk_bf16_f32 v133, v146, v148
	v_cvt_pk_bf16_f32 v134, v147, v151
	v_cvt_pk_bf16_f32 v135, v178, v156
	s_and_saveexec_b64 s[0:1], s[44:45]
	v_mul_u32_u24_e32 v136, s4, v158
	v_lshl_or_b32 v136, v192, v145, v136
	v_add_u32_e32 v212, v136, v172
	v_lshl_add_u64 v[136:137], v[212:213], 1, s[52:53]
	global_store_dwordx4 v[136:137], v[132:135], off nt
	s_nop 1
	s_or_b64 exec, exec, s[0:1]
	s_or_b32 s2, s4, 1
	v_cvt_pk_bf16_f32 v127, v126, v127
	v_cvt_pk_bf16_f32 v126, v124, v125
	v_cvt_pk_bf16_f32 v124, v128, v129
	v_cvt_pk_bf16_f32 v125, v130, v131
	s_and_saveexec_b64 s[0:1], s[42:43]
	v_mul_u32_u24_e32 v128, s2, v159
	v_lshlrev_b32_e32 v129, v180, v192
	v_add3_u32 v212, v128, v129, v181
	v_lshl_add_u64 v[128:129], v[212:213], 1, s[52:53]
	global_store_dwordx4 v[128:129], v[124:127], off nt
	s_nop 1
	s_or_b64 exec, exec, s[0:1]
	v_cvt_pk_bf16_f32 v115, v114, v115
	v_cvt_pk_bf16_f32 v114, v112, v113
	v_cvt_pk_bf16_f32 v112, v116, v117
	v_cvt_pk_bf16_f32 v113, v118, v119
	s_and_saveexec_b64 s[0:1], s[44:45]
	v_mul_u32_u24_e32 v116, s2, v158
	v_lshlrev_b32_e32 v117, v145, v192
	v_add3_u32 v212, v116, v117, v172
	v_lshl_add_u64 v[116:117], v[212:213], 1, s[52:53]
	global_store_dwordx4 v[116:117], v[112:115], off nt
	s_nop 1
	s_or_b64 exec, exec, s[0:1]
	s_or_b32 s2, s4, 2
	v_cvt_pk_bf16_f32 v107, v106, v107
	v_cvt_pk_bf16_f32 v106, v104, v105
	v_cvt_pk_bf16_f32 v104, v108, v109
	v_cvt_pk_bf16_f32 v105, v110, v111
	s_and_saveexec_b64 s[0:1], s[42:43]
	v_mul_u32_u24_e32 v108, s2, v159
	v_lshl_or_b32 v108, v192, v180, v108
	v_add_u32_e32 v212, v108, v181
	v_lshl_add_u64 v[108:109], v[212:213], 1, s[52:53]
	global_store_dwordx4 v[108:109], v[104:107], off nt
	s_nop 1
	s_or_b64 exec, exec, s[0:1]
	v_cvt_pk_bf16_f32 v95, v94, v95
	v_cvt_pk_bf16_f32 v94, v92, v93
	v_cvt_pk_bf16_f32 v92, v96, v97
	v_cvt_pk_bf16_f32 v93, v98, v99
	s_and_saveexec_b64 s[0:1], s[44:45]
	v_mul_u32_u24_e32 v96, s2, v158
	v_lshl_or_b32 v96, v192, v145, v96
	v_add_u32_e32 v212, v96, v172
	v_lshl_add_u64 v[96:97], v[212:213], 1, s[52:53]
	global_store_dwordx4 v[96:97], v[92:95], off nt
	s_nop 1
	s_or_b64 exec, exec, s[0:1]
	s_or_b32 s2, s4, 3
	v_cvt_pk_bf16_f32 v87, v86, v87
	v_cvt_pk_bf16_f32 v86, v84, v85
	v_cvt_pk_bf16_f32 v84, v88, v89
	v_cvt_pk_bf16_f32 v85, v90, v91
	s_and_saveexec_b64 s[0:1], s[42:43]
	v_mul_u32_u24_e32 v88, s2, v159
	v_lshlrev_b32_e32 v89, v180, v192
	v_add3_u32 v212, v88, v89, v181
	v_lshl_add_u64 v[88:89], v[212:213], 1, s[52:53]
	global_store_dwordx4 v[88:89], v[84:87], off nt
	s_nop 1
	s_or_b64 exec, exec, s[0:1]
	v_cvt_pk_bf16_f32 v75, v74, v75
	v_cvt_pk_bf16_f32 v74, v72, v73
	v_cvt_pk_bf16_f32 v72, v76, v77
	v_cvt_pk_bf16_f32 v73, v78, v79
	s_and_saveexec_b64 s[0:1], s[44:45]
	v_mul_u32_u24_e32 v76, s2, v158
	v_lshlrev_b32_e32 v77, v145, v192
	v_add3_u32 v212, v76, v77, v172
	v_lshl_add_u64 v[76:77], v[212:213], 1, s[52:53]
	global_store_dwordx4 v[76:77], v[72:75], off nt
	s_nop 1
	s_or_b64 exec, exec, s[0:1]
	s_mov_b64 s[0:1], -1
	s_addk_i32 s8, 0x80
	s_lshr_b32 s0, s8, 4
	s_and_b32 s2, s0, 0xfc
	v_cvt_pk_bf16_f32 v67, v66, v67
	v_cvt_pk_bf16_f32 v66, v64, v65
	v_cvt_pk_bf16_f32 v64, v68, v69
	v_cvt_pk_bf16_f32 v65, v70, v71
	s_and_saveexec_b64 s[0:1], s[42:43]
	v_mul_u32_u24_e32 v68, s2, v159
	v_lshl_or_b32 v68, v192, v180, v68
	v_add_u32_e32 v212, v68, v181
	v_lshl_add_u64 v[68:69], v[212:213], 1, s[52:53]
	global_store_dwordx4 v[68:69], v[64:67], off nt
	s_nop 1
	s_or_b64 exec, exec, s[0:1]
	v_cvt_pk_bf16_f32 v55, v54, v55
	v_cvt_pk_bf16_f32 v54, v52, v53
	v_cvt_pk_bf16_f32 v52, v56, v57
	v_cvt_pk_bf16_f32 v53, v58, v59
	s_and_saveexec_b64 s[0:1], s[44:45]
	v_mul_u32_u24_e32 v56, s2, v158
	v_lshl_or_b32 v56, v192, v145, v56
	v_add_u32_e32 v212, v56, v172
	v_lshl_add_u64 v[56:57], v[212:213], 1, s[52:53]
	global_store_dwordx4 v[56:57], v[52:55], off nt
	s_nop 1
	s_or_b64 exec, exec, s[0:1]
	s_or_b32 s4, s2, 1
	v_cvt_pk_bf16_f32 v47, v46, v47
	v_cvt_pk_bf16_f32 v46, v44, v45
	v_cvt_pk_bf16_f32 v44, v48, v49
	v_cvt_pk_bf16_f32 v45, v50, v51
	s_and_saveexec_b64 s[0:1], s[42:43]
	v_mul_u32_u24_e32 v48, s4, v159
	v_lshlrev_b32_e32 v49, v180, v192
	v_add3_u32 v212, v48, v49, v181
	v_lshl_add_u64 v[48:49], v[212:213], 1, s[52:53]
	global_store_dwordx4 v[48:49], v[44:47], off nt
	s_nop 1
	s_or_b64 exec, exec, s[0:1]
	v_cvt_pk_bf16_f32 v35, v34, v35
	v_cvt_pk_bf16_f32 v34, v32, v33
	v_cvt_pk_bf16_f32 v32, v36, v37
	v_cvt_pk_bf16_f32 v33, v38, v39
	s_and_saveexec_b64 s[0:1], s[44:45]
	v_mul_u32_u24_e32 v36, s4, v158
	v_lshlrev_b32_e32 v37, v145, v192
	v_add3_u32 v212, v36, v37, v172
	v_lshl_add_u64 v[36:37], v[212:213], 1, s[52:53]
	global_store_dwordx4 v[36:37], v[32:35], off nt
	s_nop 1
	s_or_b64 exec, exec, s[0:1]
	s_or_b32 s4, s2, 2
	v_cvt_pk_bf16_f32 v27, v26, v27
	v_cvt_pk_bf16_f32 v26, v24, v25
	v_cvt_pk_bf16_f32 v24, v28, v29
	v_cvt_pk_bf16_f32 v25, v30, v31
	s_and_saveexec_b64 s[0:1], s[42:43]
	v_mul_u32_u24_e32 v28, s4, v159
	v_lshl_or_b32 v28, v192, v180, v28
	v_add_u32_e32 v212, v28, v181
	v_lshl_add_u64 v[28:29], v[212:213], 1, s[52:53]
	global_store_dwordx4 v[28:29], v[24:27], off nt
	s_nop 1
	s_or_b64 exec, exec, s[0:1]
	v_cvt_pk_bf16_f32 v19, v18, v19
	v_cvt_pk_bf16_f32 v18, v16, v17
	v_cvt_pk_bf16_f32 v16, v20, v21
	v_cvt_pk_bf16_f32 v17, v22, v23
	s_and_saveexec_b64 s[0:1], s[44:45]
	v_mul_u32_u24_e32 v20, s4, v158
	v_lshl_or_b32 v20, v192, v145, v20
	v_add_u32_e32 v212, v20, v172
	v_lshl_add_u64 v[20:21], v[212:213], 1, s[52:53]
	global_store_dwordx4 v[20:21], v[16:19], off nt
	s_nop 1
	s_or_b64 exec, exec, s[0:1]
	s_or_b32 s2, s2, 3
	v_cvt_pk_bf16_f32 v11, v10, v11
	v_cvt_pk_bf16_f32 v10, v8, v9
	v_cvt_pk_bf16_f32 v8, v12, v13
	v_cvt_pk_bf16_f32 v9, v14, v15
	s_and_saveexec_b64 s[0:1], s[42:43]
	v_mul_u32_u24_e32 v12, s2, v159
	v_lshlrev_b32_e32 v13, v180, v192
	v_add3_u32 v212, v12, v13, v181
	v_lshl_add_u64 v[12:13], v[212:213], 1, s[52:53]
	global_store_dwordx4 v[12:13], v[8:11], off nt
	s_nop 1
	s_or_b64 exec, exec, s[0:1]
	s_and_b64 vcc, exec, s[38:39]
	v_cvt_pk_bf16_f32 v3, v2, v3
	v_cvt_pk_bf16_f32 v2, v0, v1
	v_cvt_pk_bf16_f32 v0, v4, v5
	v_cvt_pk_bf16_f32 v1, v6, v7
	s_and_saveexec_b64 s[0:1], s[44:45]
	v_mul_u32_u24_e32 v4, s2, v158
	v_lshlrev_b32_e32 v5, v145, v192
	v_add3_u32 v212, v4, v5, v172
	v_lshl_add_u64 v[4:5], v[212:213], 1, s[52:53]
	global_store_dwordx4 v[4:5], v[0:3], off nt
	s_nop 1
	s_branch .LBB0_464
.Lepiz_m1:
	s_and_b64 vcc, exec, s[80:81]
	v_or_b32_e32 v62, s8, v192
	v_lshlrev_b32_e32 v40, 2, v40
	v_add_lshl_u32 v212, v40, s54, 2
	v_lshlrev_b32_e32 v42, 8, v62
	v_lshl_add_u64 v[40:41], s[50:51], 0, v[212:213]
	v_and_b32_e32 v212, 0xfcf00, v42
	v_lshl_add_u64 v[42:43], v[40:41], 0, v[212:213]
	v_add_co_u32_e32 v60, vcc, 0x1000, v42
	s_movk_i32 s0, 0x2000
	s_nop 0
	v_addc_co_u32_e32 v61, vcc, 0, v43, vcc
	global_load_dwordx4 v[156:159], v[42:43], off
	global_load_dwordx4 v[152:155], v[60:61], off
	v_add_co_u32_e32 v60, vcc, s0, v42
	s_nop 1
	v_addc_co_u32_e32 v61, vcc, 0, v43, vcc
	v_add_co_u32_e32 v42, vcc, 0x3000, v42
	s_nop 1
	v_addc_co_u32_e32 v43, vcc, 0, v43, vcc
	global_load_dwordx4 v[140:143], v[60:61], off
	global_load_dwordx4 v[120:123], v[42:43], off
	v_mov_b32_e32 v42, 0x2000
	v_lshl_add_u32 v42, v62, 6, v42
	v_and_b32_e32 v42, 0x3f3c0, v42
	v_lshlrev_b32_e32 v212, 2, v42
	v_lshl_add_u64 v[40:41], v[40:41], 0, v[212:213]
	v_add_co_u32_e32 v42, vcc, s0, v40
	s_movk_i32 s0, 0x3000
	s_nop 0
	v_addc_co_u32_e32 v43, vcc, 0, v41, vcc
	global_load_dwordx4 v[80:83], v[42:43], off offset:-4096
	global_load_dwordx4 v[60:63], v[42:43], off
	v_add_co_u32_e32 v42, vcc, s0, v40
	s_mov_b64 s[0:1], 0
	s_nop 0
	v_addc_co_u32_e32 v43, vcc, 0, v41, vcc
	global_load_dwordx4 v[100:103], v[40:41], off
	s_nop 0
	global_load_dwordx4 v[40:43], v[42:43], off
	v_cndmask_b32_e64 v172, 0, 1, s[80:81]
	v_cmp_ne_u32_e64 s[40:41], 1, v172
	s_waitcnt vmcnt(0)
	v_cvt_f32_f16_e32 v174, v156
	v_cvt_f32_f16_e32 v175, v157
	v_cvt_f32_f16_e32 v172, v158
	v_cvt_f32_f16_e32 v173, v159
	v_cvt_f32_f16_sdwa v176, v156 dst_sel:DWORD dst_unused:UNUSED_PAD src0_sel:WORD_1
	v_cvt_f32_f16_sdwa v177, v157 dst_sel:DWORD dst_unused:UNUSED_PAD src0_sel:WORD_1
	v_cvt_f32_f16_sdwa v158, v158 dst_sel:DWORD dst_unused:UNUSED_PAD src0_sel:WORD_1
	v_cvt_f32_f16_sdwa v157, v159 dst_sel:DWORD dst_unused:UNUSED_PAD src0_sel:WORD_1
	v_pk_mul_f32 v[206:207], v[148:149], v[176:177] op_sel:[1,0] op_sel_hi:[0,0]
	v_mov_b32_e32 v180, v175
	v_mov_b32_e32 v181, v177
	v_mul_f32_e32 v156, v151, v177
	v_pk_fma_f32 v[178:179], v[148:149], v[174:175], v[206:207] op_sel_hi:[1,0,1]
	v_pk_fma_f32 v[180:181], v[150:151], v[180:181], v[156:157] op_sel_hi:[1,1,0] neg_lo:[0,0,1] neg_hi:[0,0,1]
	v_mov_b32_e32 v182, v177
	v_mov_b32_e32 v183, v175
	v_mul_f32_e32 v156, v151, v175
	v_pk_fma_f32 v[182:183], v[150:151], v[182:183], v[156:157] op_sel_hi:[1,1,0]
	v_mov_b32_e32 v156, v173
	v_mul_f32_e32 v178, v147, v157
	v_pk_mul_f32 v[208:209], v[148:149], v[174:175]
	v_pk_mul_f32 v[210:211], v[144:145], v[158:159] op_sel:[1,0] op_sel_hi:[0,0]
	v_pk_mul_f32 v[224:225], v[144:145], v[172:173]
	v_pk_fma_f32 v[186:187], v[146:147], v[156:157], v[178:179] op_sel_hi:[1,1,0] neg_lo:[0,0,1] neg_hi:[0,0,1]
	v_mov_b32_e32 v188, v157
	v_mov_b32_e32 v189, v173
	v_mul_f32_e32 v156, v147, v173
	v_pk_fma_f32 v[184:185], v[144:145], v[172:173], v[210:211] op_sel_hi:[1,0,1]
	v_pk_fma_f32 v[188:189], v[146:147], v[188:189], v[156:157] op_sel_hi:[1,1,0]
	v_sub_f32_e32 v156, v208, v206
	v_sub_f32_e32 v178, v224, v210
	s_mov_b64 s[4:5], 0
	v_cndmask_b32_e64 v159, 0, 1, s[0:1]
	v_cmp_ne_u32_e64 s[38:39], 1, v159
	s_lshr_b32 s0, s8, 4
	s_and_b32 s4, s0, 0xfc
	s_ashr_i32 s0, s2, 31
	s_lshr_b32 s0, s0, 28
	s_add_i32 s0, s2, s0
	s_ashr_i32 s13, s0, 4
	v_add_u32_e32 v144, v204, v201
	s_movk_i32 s0, 0x300
	v_mul_lo_u32 v144, v144, s0
	v_sub_u32_e32 v144, v193, v144
	v_cndmask_b32_e64 v146, v203, v144, s[42:43]
	v_lshrrev_b32_e32 v144, 7, v146
	v_mad_u64_u32 v[144:145], s[0:1], v202, s13, v[144:145]
	v_lshlrev_b32_e32 v145, 4, v146
	v_lshl_add_u32 v144, v144, 19, v200
	v_and_b32_e32 v145, 0x600, v145
	v_and_b32_e32 v146, 31, v146
	v_or3_b32 v146, v144, v145, v146
	v_add_u32_e32 v144, 0xfffff200, v193
	v_mul_hi_i32 v145, v144, s6
	v_lshrrev_b32_e32 v147, 31, v145
	v_ashrrev_i32_e32 v145, 6, v145
	v_add_u32_e32 v145, v145, v147
	v_mul_i32_i24_e32 v147, 0x180, v145
	v_sub_u32_e32 v144, v144, v147
	v_mul_i32_i24_e32 v147, 0x2aab, v144
	v_mov_b32_e32 v148, 4
	v_ashrrev_i16_sdwa v148, v148, v147 dst_sel:DWORD dst_unused:UNUSED_PAD src0_sel:DWORD src1_sel:WORD_1
	v_lshrrev_b32_e32 v147, 31, v147
	v_add_u16_e32 v147, v148, v147
	v_mul_lo_u16_e32 v148, 0x60, v147
	v_sub_u16_e32 v144, v144, v148
	s_lshl_b32 s5, s13, 2
	v_bfe_i32 v148, v144, 0, 16
	v_mul_i32_i24_e32 v144, 0x600000, v145
	v_and_or_b32 v144, v148, 31, v144
	v_add_u32_e32 v145, s5, v147
	s_mov_b32 s0, 0x60000
	v_lshlrev_b32_e32 v147, 4, v148
	v_mad_u64_u32 v[144:145], s[0:1], v145, s0, v[144:145]
	v_and_b32_e32 v147, 0xfffffe00, v147
	s_mov_b32 s0, 0x3800000
	v_add3_u32 v147, v144, v147, s0
	v_add_u32_e32 v144, 0xffffef00, v193
	v_mul_hi_i32 v145, v144, s6
	v_lshrrev_b32_e32 v148, 31, v145
	v_ashrrev_i32_e32 v145, 7, v145
	v_add_u32_e32 v145, v145, v148
	v_mul_i32_i24_e32 v148, 0x300, v145
	v_sub_u32_e32 v144, v144, v148
	v_mul_i32_i24_e32 v148, 0x2aab, v144
	v_mov_b32_e32 v149, 5
	v_ashrrev_i16_sdwa v149, v149, v148 dst_sel:DWORD dst_unused:UNUSED_PAD src0_sel:DWORD src1_sel:WORD_1
	v_lshrrev_b32_e32 v148, 31, v148
	v_add_u16_e32 v148, v149, v148
	v_mul_lo_u16_e32 v149, 0xc0, v148
	v_sub_u16_e32 v144, v144, v149
	s_mov_b32 s0, 0xc00000
	v_bfe_i32 v149, v144, 0, 16
	v_mul_lo_u32 v144, v145, s0
	v_and_or_b32 v144, v149, 31, v144
	v_add_u32_e32 v145, s5, v148
	s_mov_b32 s0, 0xc0000
	v_lshlrev_b32_e32 v148, 4, v149
	v_mad_u64_u32 v[144:145], s[0:1], v145, s0, v[144:145]
	v_and_b32_e32 v148, 0xfffffe00, v148
	s_mov_b32 s0, 0x4400000
	v_add3_u32 v144, v144, v148, s0
	s_movk_i32 s0, 0xe00
	s_lshl_b32 s2, s13, 16
	v_cmp_gt_i32_e32 vcc, s0, v193
	s_movk_i32 s0, 0x1710
	s_add_i32 s2, s2, 0x5bfe900
	v_cmp_gt_u32_e64 s[42:43], s0, v193
	s_movk_i32 s0, 0x1700
	v_add_u32_e32 v145, s2, v193
	v_cndmask_b32_e64 v149, 0, v237, s[42:43]
	v_cmp_gt_i32_e64 s[46:47], s0, v193
	s_movk_i32 s0, 0x1100
	v_cndmask_b32_e32 v148, v236, v218, vcc
	v_cndmask_b32_e64 v149, v149, v239, s[46:47]
	v_cmp_gt_i32_e64 s[42:43], s0, v193
	v_cndmask_b32_e64 v144, v145, v144, s[46:47]
	s_nop 0
	v_cndmask_b32_e64 v159, v149, v148, s[42:43]
	v_cndmask_b32_e64 v144, v144, v147, s[42:43]
	v_cndmask_b32_e32 v181, v144, v146, vcc
	v_cvt_pk_bf16_f32 v144, v156, v179
	v_cvt_pk_bf16_f32 v145, v180, v182
	v_cmp_ne_u32_e64 s[42:43], 0, v159
	v_cndmask_b32_e64 v180, 4, 5, s[46:47]
	v_cvt_pk_bf16_f32 v146, v178, v185
	v_cvt_pk_bf16_f32 v147, v186, v188
	s_and_saveexec_b64 s[0:1], s[42:43]
	v_mul_u32_u24_e32 v148, s4, v159
	v_lshl_or_b32 v148, v192, v180, v148
	v_add_u32_e32 v212, v148, v181
	v_lshl_add_u64 v[148:149], v[212:213], 1, s[52:53]
	global_store_dwordx4 v[148:149], v[144:147], off nt
	s_nop 1
	s_or_b64 exec, exec, s[0:1]
	s_mov_b64 s[0:1], -1
	v_pk_mul_f32 v[182:183], v[136:137], v[176:177] op_sel:[1,0] op_sel_hi:[0,0]
	v_pk_fma_f32 v[144:145], v[136:137], v[174:175], v[182:183] op_sel_hi:[1,0,1]
	v_mov_b32_e32 v176, v175
	v_mul_f32_e32 v144, v139, v177
	v_pk_mul_f32 v[184:185], v[136:137], v[174:175]
	v_pk_fma_f32 v[146:147], v[138:139], v[176:177], v[144:145] op_sel_hi:[1,1,0] neg_lo:[0,0,1] neg_hi:[0,0,1]
	v_mov_b32_e32 v174, v177
	v_mul_f32_e32 v144, v139, v175
	v_pk_fma_f32 v[148:149], v[138:139], v[174:175], v[144:145] op_sel_hi:[1,1,0]
	v_pk_mul_f32 v[174:175], v[132:133], v[158:159] op_sel:[1,0] op_sel_hi:[0,0]
	v_mov_b32_e32 v156, v173
	v_mul_f32_e32 v144, v135, v157
	v_pk_mul_f32 v[176:177], v[132:133], v[172:173]
	v_pk_fma_f32 v[150:151], v[132:133], v[172:173], v[174:175] op_sel_hi:[1,0,1]
	v_pk_fma_f32 v[178:179], v[134:135], v[156:157], v[144:145] op_sel_hi:[1,1,0] neg_lo:[0,0,1] neg_hi:[0,0,1]
	v_mov_b32_e32 v172, v157
	v_mul_f32_e32 v144, v135, v173
	v_pk_fma_f32 v[156:157], v[134:135], v[172:173], v[144:145] op_sel_hi:[1,1,0]
	v_sub_f32_e32 v144, v184, v182
	v_sub_f32_e32 v147, v176, v174
	v_add_u32_e32 v132, v198, v197
	s_movk_i32 s0, 0x300
	v_mul_lo_u32 v132, v132, s0
	v_sub_u32_e32 v132, v194, v132
	v_cndmask_b32_e64 v134, v199, v132, s[44:45]
	v_lshrrev_b32_e32 v132, 7, v134
	v_mad_u64_u32 v[132:133], s[0:1], v195, s13, v[132:133]
	v_lshlrev_b32_e32 v133, 4, v134
	v_lshl_add_u32 v132, v132, 19, v196
	v_and_b32_e32 v133, 0x600, v133
	v_and_b32_e32 v134, 31, v134
	v_or3_b32 v134, v132, v133, v134
	v_add_u32_e32 v132, 0xfffff280, v193
	v_mul_hi_i32 v133, v132, s6
	v_lshrrev_b32_e32 v135, 31, v133
	v_ashrrev_i32_e32 v133, 6, v133
	v_add_u32_e32 v133, v133, v135
	v_mul_i32_i24_e32 v135, 0x180, v133
	v_sub_u32_e32 v132, v132, v135
	v_mul_i32_i24_e32 v135, 0x2aab, v132
	v_lshrrev_b32_e32 v136, 31, v135
	v_ashrrev_i32_e32 v135, 20, v135
	v_add_u16_e32 v135, v135, v136
	v_mul_lo_u16_e32 v136, 0x60, v135
	v_sub_u16_e32 v132, v132, v136
	v_bfe_i32 v136, v132, 0, 16
	v_mul_i32_i24_e32 v132, 0x600000, v133
	v_and_or_b32 v132, v136, 31, v132
	v_add_u32_e32 v133, s5, v135
	s_mov_b32 s0, 0x60000
	v_lshlrev_b32_e32 v135, 4, v136
	v_mad_u64_u32 v[132:133], s[0:1], v133, s0, v[132:133]
	v_and_b32_e32 v135, 0xfffffe00, v135
	s_mov_b32 s0, 0x3800000
	v_add3_u32 v135, v132, v135, s0
	v_add_u32_e32 v132, 0xffffef80, v193
	v_mul_hi_i32 v133, v132, s6
	v_lshrrev_b32_e32 v136, 31, v133
	v_ashrrev_i32_e32 v133, 7, v133
	v_add_u32_e32 v133, v133, v136
	v_mul_i32_i24_e32 v136, 0x300, v133
	v_sub_u32_e32 v132, v132, v136
	v_mul_i32_i24_e32 v136, 0x2aab, v132
	v_lshrrev_b32_e32 v137, 31, v136
	v_ashrrev_i32_e32 v136, 21, v136
	v_add_u16_e32 v136, v136, v137
	v_mul_lo_u16_e32 v137, 0xc0, v136
	v_sub_u16_e32 v132, v132, v137
	s_mov_b32 s0, 0xc00000
	v_bfe_i32 v137, v132, 0, 16
	v_mul_lo_u32 v132, v133, s0
	v_and_or_b32 v132, v137, 31, v132
	v_add_u32_e32 v133, s5, v136
	s_mov_b32 s0, 0xc0000
	v_lshlrev_b32_e32 v136, 4, v137
	v_mad_u64_u32 v[132:133], s[0:1], v133, s0, v[132:133]
	v_and_b32_e32 v136, 0xfffffe00, v136
	s_mov_b32 s0, 0x4400000
	v_add3_u32 v132, v132, v136, s0
	s_movk_i32 s0, 0xd80
	v_cmp_gt_i32_e32 vcc, s0, v193
	s_movk_i32 s0, 0x1710
	v_cmp_gt_u32_e64 s[44:45], s0, v194
	s_movk_i32 s0, 0x1680
	v_add_u32_e32 v133, s2, v194
	v_cndmask_b32_e64 v137, 0, v237, s[44:45]
	v_cmp_gt_i32_e64 s[46:47], s0, v193
	s_movk_i32 s0, 0x1080
	v_cndmask_b32_e32 v136, v236, v218, vcc
	v_cndmask_b32_e64 v137, v137, v239, s[46:47]
	v_cmp_gt_i32_e64 s[44:45], s0, v193
	v_cndmask_b32_e64 v132, v133, v132, s[46:47]
	s_nop 0
	v_cndmask_b32_e64 v158, v137, v136, s[44:45]
	v_cndmask_b32_e64 v132, v132, v135, s[44:45]
	v_cndmask_b32_e32 v172, v132, v134, vcc
	v_cvt_pk_bf16_f32 v132, v144, v145
	v_cmp_ne_u32_e64 s[44:45], 0, v158
	v_cndmask_b32_e64 v145, 4, 5, s[46:47]
	v_cvt_pk_bf16_f32 v133, v146, v148
	v_cvt_pk_bf16_f32 v134, v147, v151
	v_cvt_pk_bf16_f32 v135, v178, v156
	s_and_saveexec_b64 s[0:1], s[44:45]
	v_mul_u32_u24_e32 v136, s4, v158
	v_lshl_or_b32 v136, v192, v145, v136
	v_add_u32_e32 v212, v136, v172
	v_lshl_add_u64 v[136:137], v[212:213], 1, s[52:53]
	global_store_dwordx4 v[136:137], v[132:135], off nt
	s_nop 1
	s_or_b64 exec, exec, s[0:1]
	v_cvt_f32_f16_e32 v136, v152
	v_cvt_f32_f16_e32 v137, v153
	v_cvt_f32_f16_e32 v132, v154
	v_cvt_f32_f16_e32 v133, v155
	v_cvt_f32_f16_sdwa v138, v152 dst_sel:DWORD dst_unused:UNUSED_PAD src0_sel:WORD_1
	v_cvt_f32_f16_sdwa v139, v153 dst_sel:DWORD dst_unused:UNUSED_PAD src0_sel:WORD_1
	v_cvt_f32_f16_sdwa v144, v154 dst_sel:DWORD dst_unused:UNUSED_PAD src0_sel:WORD_1
	v_cvt_f32_f16_sdwa v135, v155 dst_sel:DWORD dst_unused:UNUSED_PAD src0_sel:WORD_1
	v_pk_mul_f32 v[174:175], v[128:129], v[138:139] op_sel:[1,0] op_sel_hi:[0,0]
	v_mov_b32_e32 v148, v137
	v_mov_b32_e32 v149, v139
	v_mul_f32_e32 v134, v131, v139
	v_pk_fma_f32 v[146:147], v[128:129], v[136:137], v[174:175] op_sel_hi:[1,0,1]
	v_pk_fma_f32 v[148:149], v[130:131], v[148:149], v[134:135] op_sel_hi:[1,1,0] neg_lo:[0,0,1] neg_hi:[0,0,1]
	v_mov_b32_e32 v150, v139
	v_mov_b32_e32 v151, v137
	v_mul_f32_e32 v134, v131, v137
	v_pk_fma_f32 v[150:151], v[130:131], v[150:151], v[134:135] op_sel_hi:[1,1,0]
	v_mov_b32_e32 v134, v133
	v_mul_f32_e32 v146, v127, v135
	v_pk_mul_f32 v[176:177], v[128:129], v[136:137]
	v_pk_mul_f32 v[178:179], v[124:125], v[144:145] op_sel:[1,0] op_sel_hi:[0,0]
	v_pk_mul_f32 v[182:183], v[124:125], v[132:133]
	v_pk_fma_f32 v[154:155], v[126:127], v[134:135], v[146:147] op_sel_hi:[1,1,0] neg_lo:[0,0,1] neg_hi:[0,0,1]
	v_mov_b32_e32 v156, v135
	v_mov_b32_e32 v157, v133
	v_mul_f32_e32 v134, v127, v133
	v_pk_fma_f32 v[152:153], v[124:125], v[132:133], v[178:179] op_sel_hi:[1,0,1]
	v_pk_fma_f32 v[156:157], v[126:127], v[156:157], v[134:135] op_sel_hi:[1,1,0]
	v_sub_f32_e32 v134, v176, v174
	v_sub_f32_e32 v146, v182, v178
	s_or_b32 s2, s4, 1
	v_cvt_pk_bf16_f32 v124, v134, v147
	v_cvt_pk_bf16_f32 v125, v148, v150
	v_cvt_pk_bf16_f32 v126, v146, v153
	v_cvt_pk_bf16_f32 v127, v154, v156
	s_and_saveexec_b64 s[0:1], s[42:43]
	v_mul_u32_u24_e32 v128, s2, v159
	v_lshlrev_b32_e32 v129, v180, v192
	v_add3_u32 v212, v128, v129, v181
	v_lshl_add_u64 v[128:129], v[212:213], 1, s[52:53]
	global_store_dwordx4 v[128:129], v[124:127], off nt
	s_nop 1
	s_or_b64 exec, exec, s[0:1]
	v_pk_mul_f32 v[148:149], v[116:117], v[138:139] op_sel:[1,0] op_sel_hi:[0,0]
	v_pk_fma_f32 v[124:125], v[116:117], v[136:137], v[148:149] op_sel_hi:[1,0,1]
	v_mov_b32_e32 v138, v137
	v_mul_f32_e32 v124, v119, v139
	v_pk_mul_f32 v[150:151], v[116:117], v[136:137]
	v_pk_fma_f32 v[126:127], v[118:119], v[138:139], v[124:125] op_sel_hi:[1,1,0] neg_lo:[0,0,1] neg_hi:[0,0,1]
	v_mov_b32_e32 v136, v139
	v_mul_f32_e32 v124, v119, v137
	v_pk_fma_f32 v[128:129], v[118:119], v[136:137], v[124:125] op_sel_hi:[1,1,0]
	v_pk_mul_f32 v[136:137], v[112:113], v[144:145] op_sel:[1,0] op_sel_hi:[0,0]
	v_mov_b32_e32 v134, v133
	v_mul_f32_e32 v124, v115, v135
	v_pk_mul_f32 v[138:139], v[112:113], v[132:133]
	v_pk_fma_f32 v[130:131], v[112:113], v[132:133], v[136:137] op_sel_hi:[1,0,1]
	v_pk_fma_f32 v[146:147], v[114:115], v[134:135], v[124:125] op_sel_hi:[1,1,0] neg_lo:[0,0,1] neg_hi:[0,0,1]
	v_mov_b32_e32 v132, v135
	v_mul_f32_e32 v124, v115, v133
	v_pk_fma_f32 v[134:135], v[114:115], v[132:133], v[124:125] op_sel_hi:[1,1,0]
	v_sub_f32_e32 v124, v150, v148
	v_sub_f32_e32 v127, v138, v136
	v_cvt_pk_bf16_f32 v112, v124, v125
	v_cvt_pk_bf16_f32 v113, v126, v128
	v_cvt_pk_bf16_f32 v114, v127, v131
	v_cvt_pk_bf16_f32 v115, v146, v134
	s_and_saveexec_b64 s[0:1], s[44:45]
	v_mul_u32_u24_e32 v116, s2, v158
	v_lshlrev_b32_e32 v117, v145, v192
	v_add3_u32 v212, v116, v117, v172
	v_lshl_add_u64 v[116:117], v[212:213], 1, s[52:53]
	global_store_dwordx4 v[116:117], v[112:115], off nt
	s_nop 1
	s_or_b64 exec, exec, s[0:1]
	v_cvt_f32_f16_e32 v116, v140
	v_cvt_f32_f16_e32 v117, v141
	v_cvt_f32_f16_e32 v112, v142
	v_cvt_f32_f16_e32 v113, v143
	v_cvt_f32_f16_sdwa v118, v140 dst_sel:DWORD dst_unused:UNUSED_PAD src0_sel:WORD_1
	v_cvt_f32_f16_sdwa v119, v141 dst_sel:DWORD dst_unused:UNUSED_PAD src0_sel:WORD_1
	v_cvt_f32_f16_sdwa v124, v142 dst_sel:DWORD dst_unused:UNUSED_PAD src0_sel:WORD_1
	v_cvt_f32_f16_sdwa v115, v143 dst_sel:DWORD dst_unused:UNUSED_PAD src0_sel:WORD_1
	v_pk_mul_f32 v[138:139], v[108:109], v[118:119] op_sel:[1,0] op_sel_hi:[0,0]
	v_mov_b32_e32 v128, v117
	v_mov_b32_e32 v129, v119
	v_mul_f32_e32 v114, v111, v119
	v_pk_fma_f32 v[126:127], v[108:109], v[116:117], v[138:139] op_sel_hi:[1,0,1]
	v_pk_fma_f32 v[128:129], v[110:111], v[128:129], v[114:115] op_sel_hi:[1,1,0] neg_lo:[0,0,1] neg_hi:[0,0,1]
	v_mov_b32_e32 v130, v119
	v_mov_b32_e32 v131, v117
	v_mul_f32_e32 v114, v111, v117
	v_pk_fma_f32 v[130:131], v[110:111], v[130:131], v[114:115] op_sel_hi:[1,1,0]
	v_mov_b32_e32 v114, v113
	v_mul_f32_e32 v126, v107, v115
	v_pk_mul_f32 v[140:141], v[108:109], v[116:117]
	v_pk_mul_f32 v[142:143], v[104:105], v[124:125] op_sel:[1,0] op_sel_hi:[0,0]
	v_pk_mul_f32 v[146:147], v[104:105], v[112:113]
	v_pk_fma_f32 v[134:135], v[106:107], v[114:115], v[126:127] op_sel_hi:[1,1,0] neg_lo:[0,0,1] neg_hi:[0,0,1]
	v_mov_b32_e32 v136, v115
	v_mov_b32_e32 v137, v113
	v_mul_f32_e32 v114, v107, v113
	v_pk_fma_f32 v[132:133], v[104:105], v[112:113], v[142:143] op_sel_hi:[1,0,1]
	v_pk_fma_f32 v[136:137], v[106:107], v[136:137], v[114:115] op_sel_hi:[1,1,0]
	v_sub_f32_e32 v114, v140, v138
	v_sub_f32_e32 v125, v146, v142
	s_or_b32 s2, s4, 2
	v_cvt_pk_bf16_f32 v104, v114, v127
	v_cvt_pk_bf16_f32 v105, v128, v130
	v_cvt_pk_bf16_f32 v106, v125, v133
	v_cvt_pk_bf16_f32 v107, v134, v136
	s_and_saveexec_b64 s[0:1], s[42:43]
	v_mul_u32_u24_e32 v108, s2, v159
	v_lshl_or_b32 v108, v192, v180, v108
	v_add_u32_e32 v212, v108, v181
	v_lshl_add_u64 v[108:109], v[212:213], 1, s[52:53]
	global_store_dwordx4 v[108:109], v[104:107], off nt
	s_nop 1
	s_or_b64 exec, exec, s[0:1]
	v_pk_mul_f32 v[128:129], v[96:97], v[118:119] op_sel:[1,0] op_sel_hi:[0,0]
	v_pk_fma_f32 v[104:105], v[96:97], v[116:117], v[128:129] op_sel_hi:[1,0,1]
	v_mov_b32_e32 v118, v117
	v_mul_f32_e32 v104, v99, v119
	v_pk_mul_f32 v[130:131], v[96:97], v[116:117]
	v_pk_fma_f32 v[106:107], v[98:99], v[118:119], v[104:105] op_sel_hi:[1,1,0] neg_lo:[0,0,1] neg_hi:[0,0,1]
	v_mov_b32_e32 v116, v119
	v_mul_f32_e32 v104, v99, v117
	v_pk_fma_f32 v[108:109], v[98:99], v[116:117], v[104:105] op_sel_hi:[1,1,0]
	v_pk_mul_f32 v[116:117], v[92:93], v[124:125] op_sel:[1,0] op_sel_hi:[0,0]
	v_mov_b32_e32 v114, v113
	v_mul_f32_e32 v104, v95, v115
	v_pk_mul_f32 v[118:119], v[92:93], v[112:113]
	v_pk_fma_f32 v[110:111], v[92:93], v[112:113], v[116:117] op_sel_hi:[1,0,1]
	v_pk_fma_f32 v[126:127], v[94:95], v[114:115], v[104:105] op_sel_hi:[1,1,0] neg_lo:[0,0,1] neg_hi:[0,0,1]
	v_mov_b32_e32 v112, v115
	v_mul_f32_e32 v104, v95, v113
	v_pk_fma_f32 v[114:115], v[94:95], v[112:113], v[104:105] op_sel_hi:[1,1,0]
	v_sub_f32_e32 v104, v130, v128
	v_sub_f32_e32 v107, v118, v116
	v_cvt_pk_bf16_f32 v92, v104, v105
	v_cvt_pk_bf16_f32 v93, v106, v108
	v_cvt_pk_bf16_f32 v94, v107, v111
	v_cvt_pk_bf16_f32 v95, v126, v114
	s_and_saveexec_b64 s[0:1], s[44:45]
	v_mul_u32_u24_e32 v96, s2, v158
	v_lshl_or_b32 v96, v192, v145, v96
	v_add_u32_e32 v212, v96, v172
	v_lshl_add_u64 v[96:97], v[212:213], 1, s[52:53]
	global_store_dwordx4 v[96:97], v[92:95], off nt
	s_nop 1
	s_or_b64 exec, exec, s[0:1]
	v_cvt_f32_f16_e32 v96, v120
	v_cvt_f32_f16_e32 v97, v121
	v_cvt_f32_f16_e32 v92, v122
	v_cvt_f32_f16_e32 v93, v123
	v_cvt_f32_f16_sdwa v98, v120 dst_sel:DWORD dst_unused:UNUSED_PAD src0_sel:WORD_1
	v_cvt_f32_f16_sdwa v99, v121 dst_sel:DWORD dst_unused:UNUSED_PAD src0_sel:WORD_1
	v_cvt_f32_f16_sdwa v104, v122 dst_sel:DWORD dst_unused:UNUSED_PAD src0_sel:WORD_1
	v_cvt_f32_f16_sdwa v95, v123 dst_sel:DWORD dst_unused:UNUSED_PAD src0_sel:WORD_1
	v_pk_mul_f32 v[118:119], v[88:89], v[98:99] op_sel:[1,0] op_sel_hi:[0,0]
	v_mov_b32_e32 v108, v97
	v_mov_b32_e32 v109, v99
	v_mul_f32_e32 v94, v91, v99
	v_pk_fma_f32 v[106:107], v[88:89], v[96:97], v[118:119] op_sel_hi:[1,0,1]
	v_pk_fma_f32 v[108:109], v[90:91], v[108:109], v[94:95] op_sel_hi:[1,1,0] neg_lo:[0,0,1] neg_hi:[0,0,1]
	v_mov_b32_e32 v110, v99
	v_mov_b32_e32 v111, v97
	v_mul_f32_e32 v94, v91, v97
	v_pk_fma_f32 v[110:111], v[90:91], v[110:111], v[94:95] op_sel_hi:[1,1,0]
	v_mov_b32_e32 v94, v93
	v_mul_f32_e32 v106, v87, v95
	v_pk_mul_f32 v[120:121], v[88:89], v[96:97]
	v_pk_mul_f32 v[122:123], v[84:85], v[104:105] op_sel:[1,0] op_sel_hi:[0,0]
	v_pk_mul_f32 v[124:125], v[84:85], v[92:93]
	v_pk_fma_f32 v[114:115], v[86:87], v[94:95], v[106:107] op_sel_hi:[1,1,0] neg_lo:[0,0,1] neg_hi:[0,0,1]
	v_mov_b32_e32 v116, v95
	v_mov_b32_e32 v117, v93
	v_mul_f32_e32 v94, v87, v93
	v_pk_fma_f32 v[112:113], v[84:85], v[92:93], v[122:123] op_sel_hi:[1,0,1]
	v_pk_fma_f32 v[116:117], v[86:87], v[116:117], v[94:95] op_sel_hi:[1,1,0]
	v_sub_f32_e32 v94, v120, v118
	v_sub_f32_e32 v105, v124, v122
	s_or_b32 s2, s4, 3
	v_cvt_pk_bf16_f32 v84, v94, v107
	v_cvt_pk_bf16_f32 v85, v108, v110
	v_cvt_pk_bf16_f32 v86, v105, v113
	v_cvt_pk_bf16_f32 v87, v114, v116
	s_and_saveexec_b64 s[0:1], s[42:43]
	v_mul_u32_u24_e32 v88, s2, v159
	v_lshlrev_b32_e32 v89, v180, v192
	v_add3_u32 v212, v88, v89, v181
	v_lshl_add_u64 v[88:89], v[212:213], 1, s[52:53]
	global_store_dwordx4 v[88:89], v[84:87], off nt
	s_nop 1
	s_or_b64 exec, exec, s[0:1]
	v_pk_mul_f32 v[108:109], v[76:77], v[98:99] op_sel:[1,0] op_sel_hi:[0,0]
	v_pk_fma_f32 v[84:85], v[76:77], v[96:97], v[108:109] op_sel_hi:[1,0,1]
	v_mov_b32_e32 v98, v97
	v_mul_f32_e32 v84, v79, v99
	v_pk_mul_f32 v[110:111], v[76:77], v[96:97]
	v_pk_fma_f32 v[86:87], v[78:79], v[98:99], v[84:85] op_sel_hi:[1,1,0] neg_lo:[0,0,1] neg_hi:[0,0,1]
	v_mov_b32_e32 v96, v99
	v_mul_f32_e32 v84, v79, v97
	v_pk_fma_f32 v[88:89], v[78:79], v[96:97], v[84:85] op_sel_hi:[1,1,0]
	v_pk_mul_f32 v[96:97], v[72:73], v[104:105] op_sel:[1,0] op_sel_hi:[0,0]
	v_mov_b32_e32 v94, v93
	v_mul_f32_e32 v84, v75, v95
	v_pk_mul_f32 v[98:99], v[72:73], v[92:93]
	v_pk_fma_f32 v[90:91], v[72:73], v[92:93], v[96:97] op_sel_hi:[1,0,1]
	v_pk_fma_f32 v[106:107], v[74:75], v[94:95], v[84:85] op_sel_hi:[1,1,0] neg_lo:[0,0,1] neg_hi:[0,0,1]
	v_mov_b32_e32 v92, v95
	v_mul_f32_e32 v84, v75, v93
	v_pk_fma_f32 v[94:95], v[74:75], v[92:93], v[84:85] op_sel_hi:[1,1,0]
	v_sub_f32_e32 v84, v110, v108
	v_sub_f32_e32 v87, v98, v96
	v_cvt_pk_bf16_f32 v72, v84, v85
	v_cvt_pk_bf16_f32 v73, v86, v88
	v_cvt_pk_bf16_f32 v74, v87, v91
	v_cvt_pk_bf16_f32 v75, v106, v94
	s_and_saveexec_b64 s[0:1], s[44:45]
	v_mul_u32_u24_e32 v76, s2, v158
	v_lshlrev_b32_e32 v77, v145, v192
	v_add3_u32 v212, v76, v77, v172
	v_lshl_add_u64 v[76:77], v[212:213], 1, s[52:53]
	global_store_dwordx4 v[76:77], v[72:75], off nt
	s_nop 1
	s_or_b64 exec, exec, s[0:1]
	v_cvt_f32_f16_e32 v76, v100
	v_cvt_f32_f16_e32 v77, v101
	v_cvt_f32_f16_e32 v72, v102
	v_cvt_f32_f16_e32 v73, v103
	v_cvt_f32_f16_sdwa v78, v100 dst_sel:DWORD dst_unused:UNUSED_PAD src0_sel:WORD_1
	v_cvt_f32_f16_sdwa v79, v101 dst_sel:DWORD dst_unused:UNUSED_PAD src0_sel:WORD_1
	v_cvt_f32_f16_sdwa v84, v102 dst_sel:DWORD dst_unused:UNUSED_PAD src0_sel:WORD_1
	v_cvt_f32_f16_sdwa v75, v103 dst_sel:DWORD dst_unused:UNUSED_PAD src0_sel:WORD_1
	v_pk_mul_f32 v[98:99], v[68:69], v[78:79] op_sel:[1,0] op_sel_hi:[0,0]
	v_mov_b32_e32 v88, v77
	v_mov_b32_e32 v89, v79
	v_mul_f32_e32 v74, v71, v79
	v_pk_fma_f32 v[86:87], v[68:69], v[76:77], v[98:99] op_sel_hi:[1,0,1]
	v_pk_fma_f32 v[88:89], v[70:71], v[88:89], v[74:75] op_sel_hi:[1,1,0] neg_lo:[0,0,1] neg_hi:[0,0,1]
	v_mov_b32_e32 v90, v79
	v_mov_b32_e32 v91, v77
	v_mul_f32_e32 v74, v71, v77
	v_pk_fma_f32 v[90:91], v[70:71], v[90:91], v[74:75] op_sel_hi:[1,1,0]
	v_mov_b32_e32 v74, v73
	v_mul_f32_e32 v86, v67, v75
	v_pk_mul_f32 v[100:101], v[68:69], v[76:77]
	v_pk_mul_f32 v[102:103], v[64:65], v[84:85] op_sel:[1,0] op_sel_hi:[0,0]
	v_pk_mul_f32 v[104:105], v[64:65], v[72:73]
	v_pk_fma_f32 v[94:95], v[66:67], v[74:75], v[86:87] op_sel_hi:[1,1,0] neg_lo:[0,0,1] neg_hi:[0,0,1]
	v_mov_b32_e32 v96, v75
	v_mov_b32_e32 v97, v73
	v_mul_f32_e32 v74, v67, v73
	v_pk_fma_f32 v[92:93], v[64:65], v[72:73], v[102:103] op_sel_hi:[1,0,1]
	v_pk_fma_f32 v[96:97], v[66:67], v[96:97], v[74:75] op_sel_hi:[1,1,0]
	v_sub_f32_e32 v74, v100, v98
	v_sub_f32_e32 v85, v104, v102
	s_mov_b64 s[0:1], 0
	s_addk_i32 s8, 0x80
	s_lshr_b32 s0, s8, 4
	s_and_b32 s2, s0, 0xfc
	v_cvt_pk_bf16_f32 v64, v74, v87
	v_cvt_pk_bf16_f32 v65, v88, v90
	v_cvt_pk_bf16_f32 v66, v85, v93
	v_cvt_pk_bf16_f32 v67, v94, v96
	s_and_saveexec_b64 s[0:1], s[42:43]
	v_mul_u32_u24_e32 v68, s2, v159
	v_lshl_or_b32 v68, v192, v180, v68
	v_add_u32_e32 v212, v68, v181
	v_lshl_add_u64 v[68:69], v[212:213], 1, s[52:53]
	global_store_dwordx4 v[68:69], v[64:67], off nt
	s_nop 1
	s_or_b64 exec, exec, s[0:1]
	v_pk_mul_f32 v[88:89], v[56:57], v[78:79] op_sel:[1,0] op_sel_hi:[0,0]
	v_pk_fma_f32 v[64:65], v[56:57], v[76:77], v[88:89] op_sel_hi:[1,0,1]
	v_mov_b32_e32 v78, v77
	v_mul_f32_e32 v64, v59, v79
	v_pk_mul_f32 v[90:91], v[56:57], v[76:77]
	v_pk_fma_f32 v[66:67], v[58:59], v[78:79], v[64:65] op_sel_hi:[1,1,0] neg_lo:[0,0,1] neg_hi:[0,0,1]
	v_mov_b32_e32 v76, v79
	v_mul_f32_e32 v64, v59, v77
	v_pk_fma_f32 v[68:69], v[58:59], v[76:77], v[64:65] op_sel_hi:[1,1,0]
	v_pk_mul_f32 v[76:77], v[52:53], v[84:85] op_sel:[1,0] op_sel_hi:[0,0]
	v_mov_b32_e32 v74, v73
	v_mul_f32_e32 v64, v55, v75
	v_pk_mul_f32 v[78:79], v[52:53], v[72:73]
	v_pk_fma_f32 v[70:71], v[52:53], v[72:73], v[76:77] op_sel_hi:[1,0,1]
	v_pk_fma_f32 v[86:87], v[54:55], v[74:75], v[64:65] op_sel_hi:[1,1,0] neg_lo:[0,0,1] neg_hi:[0,0,1]
	v_mov_b32_e32 v72, v75
	v_mul_f32_e32 v64, v55, v73
	v_pk_fma_f32 v[74:75], v[54:55], v[72:73], v[64:65] op_sel_hi:[1,1,0]
	v_sub_f32_e32 v64, v90, v88
	v_sub_f32_e32 v67, v78, v76
	v_cvt_pk_bf16_f32 v52, v64, v65
	v_cvt_pk_bf16_f32 v53, v66, v68
	v_cvt_pk_bf16_f32 v54, v67, v71
	v_cvt_pk_bf16_f32 v55, v86, v74
	s_and_saveexec_b64 s[0:1], s[44:45]
	v_mul_u32_u24_e32 v56, s2, v158
	v_lshl_or_b32 v56, v192, v145, v56
	v_add_u32_e32 v212, v56, v172
	v_lshl_add_u64 v[56:57], v[212:213], 1, s[52:53]
	global_store_dwordx4 v[56:57], v[52:55], off nt
	s_nop 1
	s_or_b64 exec, exec, s[0:1]
	v_cvt_f32_f16_e32 v56, v80
	v_cvt_f32_f16_e32 v57, v81
	v_cvt_f32_f16_e32 v52, v82
	v_cvt_f32_f16_e32 v53, v83
	v_cvt_f32_f16_sdwa v58, v80 dst_sel:DWORD dst_unused:UNUSED_PAD src0_sel:WORD_1
	v_cvt_f32_f16_sdwa v59, v81 dst_sel:DWORD dst_unused:UNUSED_PAD src0_sel:WORD_1
	v_cvt_f32_f16_sdwa v64, v82 dst_sel:DWORD dst_unused:UNUSED_PAD src0_sel:WORD_1
	v_cvt_f32_f16_sdwa v55, v83 dst_sel:DWORD dst_unused:UNUSED_PAD src0_sel:WORD_1
	v_pk_mul_f32 v[78:79], v[48:49], v[58:59] op_sel:[1,0] op_sel_hi:[0,0]
	v_mov_b32_e32 v68, v57
	v_mov_b32_e32 v69, v59
	v_mul_f32_e32 v54, v51, v59
	v_pk_fma_f32 v[66:67], v[48:49], v[56:57], v[78:79] op_sel_hi:[1,0,1]
	v_pk_fma_f32 v[68:69], v[50:51], v[68:69], v[54:55] op_sel_hi:[1,1,0] neg_lo:[0,0,1] neg_hi:[0,0,1]
	v_mov_b32_e32 v70, v59
	v_mov_b32_e32 v71, v57
	v_mul_f32_e32 v54, v51, v57
	v_pk_fma_f32 v[70:71], v[50:51], v[70:71], v[54:55] op_sel_hi:[1,1,0]
	v_mov_b32_e32 v54, v53
	v_mul_f32_e32 v66, v47, v55
	v_pk_mul_f32 v[80:81], v[48:49], v[56:57]
	v_pk_mul_f32 v[82:83], v[44:45], v[64:65] op_sel:[1,0] op_sel_hi:[0,0]
	v_pk_mul_f32 v[84:85], v[44:45], v[52:53]
	v_pk_fma_f32 v[74:75], v[46:47], v[54:55], v[66:67] op_sel_hi:[1,1,0] neg_lo:[0,0,1] neg_hi:[0,0,1]
	v_mov_b32_e32 v76, v55
	v_mov_b32_e32 v77, v53
	v_mul_f32_e32 v54, v47, v53
	v_pk_fma_f32 v[72:73], v[44:45], v[52:53], v[82:83] op_sel_hi:[1,0,1]
	v_pk_fma_f32 v[76:77], v[46:47], v[76:77], v[54:55] op_sel_hi:[1,1,0]
	v_sub_f32_e32 v54, v80, v78
	v_sub_f32_e32 v65, v84, v82
	s_or_b32 s4, s2, 1
	v_cvt_pk_bf16_f32 v44, v54, v67
	v_cvt_pk_bf16_f32 v45, v68, v70
	v_cvt_pk_bf16_f32 v46, v65, v73
	v_cvt_pk_bf16_f32 v47, v74, v76
	s_and_saveexec_b64 s[0:1], s[42:43]
	v_mul_u32_u24_e32 v48, s4, v159
	v_lshlrev_b32_e32 v49, v180, v192
	v_add3_u32 v212, v48, v49, v181
	v_lshl_add_u64 v[48:49], v[212:213], 1, s[52:53]
	global_store_dwordx4 v[48:49], v[44:47], off nt
	s_nop 1
	s_or_b64 exec, exec, s[0:1]
	v_pk_mul_f32 v[68:69], v[36:37], v[58:59] op_sel:[1,0] op_sel_hi:[0,0]
	v_pk_fma_f32 v[44:45], v[36:37], v[56:57], v[68:69] op_sel_hi:[1,0,1]
	v_mov_b32_e32 v58, v57
	v_mul_f32_e32 v44, v39, v59
	v_pk_mul_f32 v[70:71], v[36:37], v[56:57]
	v_pk_fma_f32 v[46:47], v[38:39], v[58:59], v[44:45] op_sel_hi:[1,1,0] neg_lo:[0,0,1] neg_hi:[0,0,1]
	v_mov_b32_e32 v56, v59
	v_mul_f32_e32 v44, v39, v57
	v_pk_fma_f32 v[48:49], v[38:39], v[56:57], v[44:45] op_sel_hi:[1,1,0]
	v_pk_mul_f32 v[56:57], v[32:33], v[64:65] op_sel:[1,0] op_sel_hi:[0,0]
	v_mov_b32_e32 v54, v53
	v_mul_f32_e32 v44, v35, v55
	v_pk_mul_f32 v[58:59], v[32:33], v[52:53]
	v_pk_fma_f32 v[50:51], v[32:33], v[52:53], v[56:57] op_sel_hi:[1,0,1]
	v_pk_fma_f32 v[66:67], v[34:35], v[54:55], v[44:45] op_sel_hi:[1,1,0] neg_lo:[0,0,1] neg_hi:[0,0,1]
	v_mov_b32_e32 v52, v55
	v_mul_f32_e32 v44, v35, v53
	v_pk_fma_f32 v[54:55], v[34:35], v[52:53], v[44:45] op_sel_hi:[1,1,0]
	v_sub_f32_e32 v44, v70, v68
	v_sub_f32_e32 v47, v58, v56
	v_cvt_pk_bf16_f32 v32, v44, v45
	v_cvt_pk_bf16_f32 v33, v46, v48
	v_cvt_pk_bf16_f32 v34, v47, v51
	v_cvt_pk_bf16_f32 v35, v66, v54
	s_and_saveexec_b64 s[0:1], s[44:45]
	v_mul_u32_u24_e32 v36, s4, v158
	v_lshlrev_b32_e32 v37, v145, v192
	v_add3_u32 v212, v36, v37, v172
	v_lshl_add_u64 v[36:37], v[212:213], 1, s[52:53]
	global_store_dwordx4 v[36:37], v[32:35], off nt
	s_nop 1
	s_or_b64 exec, exec, s[0:1]
	v_cvt_f32_f16_e32 v36, v60
	v_cvt_f32_f16_e32 v37, v61
	v_cvt_f32_f16_e32 v32, v62
	v_cvt_f32_f16_e32 v33, v63
	v_cvt_f32_f16_sdwa v38, v60 dst_sel:DWORD dst_unused:UNUSED_PAD src0_sel:WORD_1
	v_cvt_f32_f16_sdwa v39, v61 dst_sel:DWORD dst_unused:UNUSED_PAD src0_sel:WORD_1
	v_cvt_f32_f16_sdwa v44, v62 dst_sel:DWORD dst_unused:UNUSED_PAD src0_sel:WORD_1
	v_cvt_f32_f16_sdwa v35, v63 dst_sel:DWORD dst_unused:UNUSED_PAD src0_sel:WORD_1
	v_pk_mul_f32 v[58:59], v[28:29], v[38:39] op_sel:[1,0] op_sel_hi:[0,0]
	v_mov_b32_e32 v48, v37
	v_mov_b32_e32 v49, v39
	v_mul_f32_e32 v34, v31, v39
	v_pk_fma_f32 v[46:47], v[28:29], v[36:37], v[58:59] op_sel_hi:[1,0,1]
	v_pk_fma_f32 v[48:49], v[30:31], v[48:49], v[34:35] op_sel_hi:[1,1,0] neg_lo:[0,0,1] neg_hi:[0,0,1]
	v_mov_b32_e32 v50, v39
	v_mov_b32_e32 v51, v37
	v_mul_f32_e32 v34, v31, v37
	v_pk_fma_f32 v[50:51], v[30:31], v[50:51], v[34:35] op_sel_hi:[1,1,0]
	v_mov_b32_e32 v34, v33
	v_mul_f32_e32 v46, v27, v35
	v_pk_mul_f32 v[60:61], v[28:29], v[36:37]
	v_pk_mul_f32 v[62:63], v[24:25], v[44:45] op_sel:[1,0] op_sel_hi:[0,0]
	v_pk_mul_f32 v[64:65], v[24:25], v[32:33]
	v_pk_fma_f32 v[54:55], v[26:27], v[34:35], v[46:47] op_sel_hi:[1,1,0] neg_lo:[0,0,1] neg_hi:[0,0,1]
	v_mov_b32_e32 v56, v35
	v_mov_b32_e32 v57, v33
	v_mul_f32_e32 v34, v27, v33
	v_pk_fma_f32 v[52:53], v[24:25], v[32:33], v[62:63] op_sel_hi:[1,0,1]
	v_pk_fma_f32 v[56:57], v[26:27], v[56:57], v[34:35] op_sel_hi:[1,1,0]
	v_sub_f32_e32 v34, v60, v58
	v_sub_f32_e32 v45, v64, v62
	s_or_b32 s4, s2, 2
	v_cvt_pk_bf16_f32 v24, v34, v47
	v_cvt_pk_bf16_f32 v25, v48, v50
	v_cvt_pk_bf16_f32 v26, v45, v53
	v_cvt_pk_bf16_f32 v27, v54, v56
	s_and_saveexec_b64 s[0:1], s[42:43]
	v_mul_u32_u24_e32 v28, s4, v159
	v_lshl_or_b32 v28, v192, v180, v28
	v_add_u32_e32 v212, v28, v181
	v_lshl_add_u64 v[28:29], v[212:213], 1, s[52:53]
	global_store_dwordx4 v[28:29], v[24:27], off nt
	s_nop 1
	s_or_b64 exec, exec, s[0:1]
	v_pk_mul_f32 v[48:49], v[20:21], v[38:39] op_sel:[1,0] op_sel_hi:[0,0]
	v_pk_fma_f32 v[24:25], v[20:21], v[36:37], v[48:49] op_sel_hi:[1,0,1]
	v_mov_b32_e32 v38, v37
	v_mul_f32_e32 v24, v23, v39
	v_pk_mul_f32 v[50:51], v[20:21], v[36:37]
	v_pk_fma_f32 v[26:27], v[22:23], v[38:39], v[24:25] op_sel_hi:[1,1,0] neg_lo:[0,0,1] neg_hi:[0,0,1]
	v_mov_b32_e32 v36, v39
	v_mul_f32_e32 v24, v23, v37
	v_pk_fma_f32 v[28:29], v[22:23], v[36:37], v[24:25] op_sel_hi:[1,1,0]
	v_pk_mul_f32 v[36:37], v[16:17], v[44:45] op_sel:[1,0] op_sel_hi:[0,0]
	v_mov_b32_e32 v34, v33
	v_mul_f32_e32 v24, v19, v35
	v_pk_mul_f32 v[38:39], v[16:17], v[32:33]
	v_pk_fma_f32 v[30:31], v[16:17], v[32:33], v[36:37] op_sel_hi:[1,0,1]
	v_pk_fma_f32 v[46:47], v[18:19], v[34:35], v[24:25] op_sel_hi:[1,1,0] neg_lo:[0,0,1] neg_hi:[0,0,1]
	v_mov_b32_e32 v32, v35
	v_mul_f32_e32 v24, v19, v33
	v_pk_fma_f32 v[34:35], v[18:19], v[32:33], v[24:25] op_sel_hi:[1,1,0]
	v_sub_f32_e32 v24, v50, v48
	v_sub_f32_e32 v27, v38, v36
	v_cvt_pk_bf16_f32 v16, v24, v25
	v_cvt_pk_bf16_f32 v17, v26, v28
	v_cvt_pk_bf16_f32 v18, v27, v31
	v_cvt_pk_bf16_f32 v19, v46, v34
	s_and_saveexec_b64 s[0:1], s[44:45]
	v_mul_u32_u24_e32 v20, s4, v158
	v_lshl_or_b32 v20, v192, v145, v20
	v_add_u32_e32 v212, v20, v172
	v_lshl_add_u64 v[20:21], v[212:213], 1, s[52:53]
	global_store_dwordx4 v[20:21], v[16:19], off nt
	s_nop 1
	s_or_b64 exec, exec, s[0:1]
	v_cvt_f32_f16_e32 v20, v40
	v_cvt_f32_f16_e32 v21, v41
	v_cvt_f32_f16_e32 v16, v42
	v_cvt_f32_f16_e32 v17, v43
	v_cvt_f32_f16_sdwa v22, v40 dst_sel:DWORD dst_unused:UNUSED_PAD src0_sel:WORD_1
	v_cvt_f32_f16_sdwa v23, v41 dst_sel:DWORD dst_unused:UNUSED_PAD src0_sel:WORD_1
	v_cvt_f32_f16_sdwa v24, v42 dst_sel:DWORD dst_unused:UNUSED_PAD src0_sel:WORD_1
	v_cvt_f32_f16_sdwa v19, v43 dst_sel:DWORD dst_unused:UNUSED_PAD src0_sel:WORD_1
	v_pk_mul_f32 v[38:39], v[12:13], v[22:23] op_sel:[1,0] op_sel_hi:[0,0]
	v_mov_b32_e32 v28, v21
	v_mov_b32_e32 v29, v23
	v_mul_f32_e32 v18, v15, v23
	v_pk_fma_f32 v[26:27], v[12:13], v[20:21], v[38:39] op_sel_hi:[1,0,1]
	v_pk_fma_f32 v[28:29], v[14:15], v[28:29], v[18:19] op_sel_hi:[1,1,0] neg_lo:[0,0,1] neg_hi:[0,0,1]
	v_mov_b32_e32 v30, v23
	v_mov_b32_e32 v31, v21
	v_mul_f32_e32 v18, v15, v21
	v_pk_fma_f32 v[30:31], v[14:15], v[30:31], v[18:19] op_sel_hi:[1,1,0]
	v_mov_b32_e32 v18, v17
	v_mul_f32_e32 v26, v11, v19
	v_pk_mul_f32 v[40:41], v[12:13], v[20:21]
	v_pk_mul_f32 v[42:43], v[8:9], v[24:25] op_sel:[1,0] op_sel_hi:[0,0]
	v_pk_mul_f32 v[44:45], v[8:9], v[16:17]
	v_pk_fma_f32 v[34:35], v[10:11], v[18:19], v[26:27] op_sel_hi:[1,1,0] neg_lo:[0,0,1] neg_hi:[0,0,1]
	v_mov_b32_e32 v36, v19
	v_mov_b32_e32 v37, v17
	v_mul_f32_e32 v18, v11, v17
	v_pk_fma_f32 v[32:33], v[8:9], v[16:17], v[42:43] op_sel_hi:[1,0,1]
	v_pk_fma_f32 v[36:37], v[10:11], v[36:37], v[18:19] op_sel_hi:[1,1,0]
	v_sub_f32_e32 v18, v40, v38
	v_sub_f32_e32 v25, v44, v42
	s_or_b32 s2, s2, 3
	v_cvt_pk_bf16_f32 v8, v18, v27
	v_cvt_pk_bf16_f32 v9, v28, v30
	v_cvt_pk_bf16_f32 v10, v25, v33
	v_cvt_pk_bf16_f32 v11, v34, v36
	s_and_saveexec_b64 s[0:1], s[42:43]
	v_mul_u32_u24_e32 v12, s2, v159
	v_lshlrev_b32_e32 v13, v180, v192
	v_add3_u32 v212, v12, v13, v181
	v_lshl_add_u64 v[12:13], v[212:213], 1, s[52:53]
	global_store_dwordx4 v[12:13], v[8:11], off nt
	s_nop 1
	s_or_b64 exec, exec, s[0:1]
	s_and_b64 vcc, exec, s[80:81]
	v_pk_mul_f32 v[28:29], v[4:5], v[22:23] op_sel:[1,0] op_sel_hi:[0,0]
	v_pk_fma_f32 v[8:9], v[4:5], v[20:21], v[28:29] op_sel_hi:[1,0,1]
	v_mov_b32_e32 v22, v21
	v_mul_f32_e32 v8, v7, v23
	v_pk_mul_f32 v[30:31], v[4:5], v[20:21]
	v_pk_fma_f32 v[10:11], v[6:7], v[22:23], v[8:9] op_sel_hi:[1,1,0] neg_lo:[0,0,1] neg_hi:[0,0,1]
	v_mov_b32_e32 v20, v23
	v_mul_f32_e32 v8, v7, v21
	v_pk_fma_f32 v[12:13], v[6:7], v[20:21], v[8:9] op_sel_hi:[1,1,0]
	v_pk_mul_f32 v[20:21], v[0:1], v[24:25] op_sel:[1,0] op_sel_hi:[0,0]
	v_mov_b32_e32 v18, v17
	v_mul_f32_e32 v8, v3, v19
	v_pk_mul_f32 v[22:23], v[0:1], v[16:17]
	v_pk_fma_f32 v[14:15], v[0:1], v[16:17], v[20:21] op_sel_hi:[1,0,1]
	v_pk_fma_f32 v[26:27], v[2:3], v[18:19], v[8:9] op_sel_hi:[1,1,0] neg_lo:[0,0,1] neg_hi:[0,0,1]
	v_mov_b32_e32 v16, v19
	v_mul_f32_e32 v8, v3, v17
	v_pk_fma_f32 v[18:19], v[2:3], v[16:17], v[8:9] op_sel_hi:[1,1,0]
	v_sub_f32_e32 v8, v30, v28
	v_sub_f32_e32 v11, v22, v20
	v_cvt_pk_bf16_f32 v0, v8, v9
	v_cvt_pk_bf16_f32 v1, v10, v12
	v_cvt_pk_bf16_f32 v2, v11, v15
	v_cvt_pk_bf16_f32 v3, v26, v18
	s_and_saveexec_b64 s[0:1], s[44:45]
	v_mul_u32_u24_e32 v4, s2, v158
	v_lshlrev_b32_e32 v5, v145, v192
	v_add3_u32 v212, v4, v5, v172
	v_lshl_add_u64 v[4:5], v[212:213], 1, s[52:53]
	global_store_dwordx4 v[4:5], v[0:3], off nt
	s_nop 1
	s_branch .LBB0_464
.Lepiz_m2:
	v_cndmask_b32_e64 v172, 0, 1, s[80:81]
	v_cmp_ne_u32_e64 s[40:41], 1, v172
	s_waitcnt vmcnt(0)
	s_mov_b64 s[4:5], -1
	v_cndmask_b32_e64 v159, 0, 1, s[0:1]
	v_cmp_ne_u32_e64 s[38:39], 1, v159
	v_mul_f32_e32 v156, 0xbfb8aa3b, v148
	v_exp_f32_e32 v156, v156
	s_nop 0
	v_add_f32_e32 v156, 1.0, v156
	v_rcp_f32_e32 v178, v156
	v_mul_f32_e32 v156, 0xbfb8aa3b, v144
	v_exp_f32_e32 v156, v156
	s_nop 0
	v_add_f32_e32 v156, 1.0, v156
	v_rcp_f32_e32 v180, v156
	v_mul_f32_e32 v156, 0xbfb8aa3b, v149
	v_exp_f32_e32 v156, v156
	s_nop 0
	v_add_f32_e32 v156, 1.0, v156
	v_rcp_f32_e32 v179, v156
	v_mul_f32_e32 v156, 0xbfb8aa3b, v145
	v_exp_f32_e32 v156, v156
	v_pk_mul_f32 v[148:149], v[148:149], v[178:179]
	v_add_f32_e32 v156, 1.0, v156
	v_rcp_f32_e32 v181, v156
	v_mul_f32_e32 v156, 0xbfb8aa3b, v150
	v_exp_f32_e32 v156, v156
	v_pk_mul_f32 v[144:145], v[144:145], v[180:181]
	v_add_f32_e32 v156, 1.0, v156
	v_rcp_f32_e32 v182, v156
	v_mul_f32_e32 v156, 0xbfb8aa3b, v146
	v_exp_f32_e32 v156, v156
	s_nop 0
	v_add_f32_e32 v156, 1.0, v156
	v_rcp_f32_e32 v184, v156
	v_mul_f32_e32 v156, 0xbfb8aa3b, v151
	v_exp_f32_e32 v156, v156
	s_nop 0
	v_add_f32_e32 v156, 1.0, v156
	v_rcp_f32_e32 v183, v156
	v_mul_f32_e32 v156, 0xbfb8aa3b, v147
	v_exp_f32_e32 v156, v156
	v_pk_mul_f32 v[150:151], v[150:151], v[182:183]
	v_add_f32_e32 v156, 1.0, v156
	v_rcp_f32_e32 v185, v156
	s_nop 0
	v_pk_mul_f32 v[146:147], v[146:147], v[184:185]
	v_mov_b32_e32 v156, v148
	v_mov_b32_e32 v179, v149
	v_mov_b32_e32 v180, v150
	v_mov_b32_e32 v182, v151
	v_mov_b32_e32 v178, v144
	v_mov_b32_e32 v185, v145
	v_mov_b32_e32 v186, v146
	v_mov_b32_e32 v188, v147
	s_lshr_b32 s0, s8, 4
	s_and_b32 s4, s0, 0xfc
	s_ashr_i32 s0, s2, 31
	s_lshr_b32 s0, s0, 28
	s_add_i32 s0, s2, s0
	s_ashr_i32 s13, s0, 4
	v_add_u32_e32 v144, v204, v201
	s_movk_i32 s0, 0x300
	v_mul_lo_u32 v144, v144, s0
	v_sub_u32_e32 v144, v193, v144
	v_cndmask_b32_e64 v146, v203, v144, s[42:43]
	v_lshrrev_b32_e32 v144, 7, v146
	v_mad_u64_u32 v[144:145], s[0:1], v202, s13, v[144:145]
	v_lshlrev_b32_e32 v145, 4, v146
	v_lshl_add_u32 v144, v144, 19, v200
	v_and_b32_e32 v145, 0x600, v145
	v_and_b32_e32 v146, 31, v146
	v_or3_b32 v146, v144, v145, v146
	v_add_u32_e32 v144, 0xfffff200, v193
	v_mul_hi_i32 v145, v144, s6
	v_lshrrev_b32_e32 v147, 31, v145
	v_ashrrev_i32_e32 v145, 6, v145
	v_add_u32_e32 v145, v145, v147
	v_mul_i32_i24_e32 v147, 0x180, v145
	v_sub_u32_e32 v144, v144, v147
	v_mul_i32_i24_e32 v147, 0x2aab, v144
	v_mov_b32_e32 v148, 4
	v_ashrrev_i16_sdwa v148, v148, v147 dst_sel:DWORD dst_unused:UNUSED_PAD src0_sel:DWORD src1_sel:WORD_1
	v_lshrrev_b32_e32 v147, 31, v147
	v_add_u16_e32 v147, v148, v147
	v_mul_lo_u16_e32 v148, 0x60, v147
	v_sub_u16_e32 v144, v144, v148
	s_lshl_b32 s5, s13, 2
	v_bfe_i32 v148, v144, 0, 16
	v_mul_i32_i24_e32 v144, 0x600000, v145
	v_and_or_b32 v144, v148, 31, v144
	v_add_u32_e32 v145, s5, v147
	s_mov_b32 s0, 0x60000
	v_lshlrev_b32_e32 v147, 4, v148
	v_mad_u64_u32 v[144:145], s[0:1], v145, s0, v[144:145]
	v_and_b32_e32 v147, 0xfffffe00, v147
	s_mov_b32 s0, 0x3800000
	v_add3_u32 v147, v144, v147, s0
	v_add_u32_e32 v144, 0xffffef00, v193
	v_mul_hi_i32 v145, v144, s6
	v_lshrrev_b32_e32 v148, 31, v145
	v_ashrrev_i32_e32 v145, 7, v145
	v_add_u32_e32 v145, v145, v148
	v_mul_i32_i24_e32 v148, 0x300, v145
	v_sub_u32_e32 v144, v144, v148
	v_mul_i32_i24_e32 v148, 0x2aab, v144
	v_mov_b32_e32 v149, 5
	v_ashrrev_i16_sdwa v149, v149, v148 dst_sel:DWORD dst_unused:UNUSED_PAD src0_sel:DWORD src1_sel:WORD_1
	v_lshrrev_b32_e32 v148, 31, v148
	v_add_u16_e32 v148, v149, v148
	v_mul_lo_u16_e32 v149, 0xc0, v148
	v_sub_u16_e32 v144, v144, v149
	s_mov_b32 s0, 0xc00000
	v_bfe_i32 v149, v144, 0, 16
	v_mul_lo_u32 v144, v145, s0
	v_and_or_b32 v144, v149, 31, v144
	v_add_u32_e32 v145, s5, v148
	s_mov_b32 s0, 0xc0000
	v_lshlrev_b32_e32 v148, 4, v149
	v_mad_u64_u32 v[144:145], s[0:1], v145, s0, v[144:145]
	v_and_b32_e32 v148, 0xfffffe00, v148
	s_mov_b32 s0, 0x4400000
	v_add3_u32 v144, v144, v148, s0
	s_movk_i32 s0, 0xe00
	s_lshl_b32 s2, s13, 16
	v_cmp_gt_i32_e32 vcc, s0, v193
	s_movk_i32 s0, 0x1710
	s_add_i32 s2, s2, 0x5bfe900
	v_cmp_gt_u32_e64 s[42:43], s0, v193
	s_movk_i32 s0, 0x1700
	v_add_u32_e32 v145, s2, v193
	v_cndmask_b32_e64 v149, 0, v237, s[42:43]
	v_cmp_gt_i32_e64 s[46:47], s0, v193
	s_movk_i32 s0, 0x1100
	v_cndmask_b32_e32 v148, v236, v218, vcc
	v_cndmask_b32_e64 v149, v149, v239, s[46:47]
	v_cmp_gt_i32_e64 s[42:43], s0, v193
	v_cndmask_b32_e64 v144, v145, v144, s[46:47]
	s_nop 0
	v_cndmask_b32_e64 v159, v149, v148, s[42:43]
	v_cndmask_b32_e64 v144, v144, v147, s[42:43]
	v_cndmask_b32_e32 v181, v144, v146, vcc
	v_cvt_pk_bf16_f32 v144, v156, v179
	v_cvt_pk_bf16_f32 v145, v180, v182
	v_cmp_ne_u32_e64 s[42:43], 0, v159
	v_cndmask_b32_e64 v180, 4, 5, s[46:47]
	v_cvt_pk_bf16_f32 v146, v178, v185
	v_cvt_pk_bf16_f32 v147, v186, v188
	s_and_saveexec_b64 s[0:1], s[42:43]
	v_mul_u32_u24_e32 v148, s4, v159
	v_lshl_or_b32 v148, v192, v180, v148
	v_add_u32_e32 v212, v148, v181
	v_lshl_add_u64 v[148:149], v[212:213], 1, s[52:53]
	global_store_dwordx4 v[148:149], v[144:147], off nt
	s_nop 1
	s_or_b64 exec, exec, s[0:1]
	s_mov_b64 s[0:1], -1
	v_mul_f32_e32 v145, 0xbfb8aa3b, v132
	v_exp_f32_e32 v145, v145
	v_mul_f32_e32 v144, 0xbfb8aa3b, v136
	v_exp_f32_e32 v144, v144
	v_mul_f32_e32 v149, 0xbfb8aa3b, v134
	v_add_f32_e32 v145, 1.0, v145
	v_rcp_f32_e32 v146, v145
	v_mul_f32_e32 v145, 0xbfb8aa3b, v137
	v_exp_f32_e32 v145, v145
	v_add_f32_e32 v144, 1.0, v144
	v_exp_f32_e32 v149, v149
	v_rcp_f32_e32 v144, v144
	v_add_f32_e32 v145, 1.0, v145
	v_rcp_f32_e32 v145, v145
	v_add_f32_e32 v149, 1.0, v149
	v_mul_f32_e32 v147, 0xbfb8aa3b, v133
	v_mul_f32_e32 v148, 0xbfb8aa3b, v138
	v_rcp_f32_e32 v150, v149
	v_mul_f32_e32 v149, 0xbfb8aa3b, v139
	v_pk_mul_f32 v[136:137], v[136:137], v[144:145]
	v_mul_f32_e32 v144, 0xbfb8aa3b, v135
	v_exp_f32_e32 v147, v147
	v_exp_f32_e32 v148, v148
	v_exp_f32_e32 v149, v149
	v_exp_f32_e32 v144, v144
	v_add_f32_e32 v147, 1.0, v147
	v_add_f32_e32 v148, 1.0, v148
	v_add_f32_e32 v149, 1.0, v149
	v_add_f32_e32 v144, 1.0, v144
	v_rcp_f32_e32 v147, v147
	v_rcp_f32_e32 v148, v148
	v_rcp_f32_e32 v149, v149
	v_rcp_f32_e32 v151, v144
	v_pk_mul_f32 v[132:133], v[132:133], v[146:147]
	v_pk_mul_f32 v[138:139], v[138:139], v[148:149]
	v_pk_mul_f32 v[134:135], v[134:135], v[150:151]
	v_mov_b32_e32 v144, v136
	v_mov_b32_e32 v145, v137
	v_mov_b32_e32 v146, v138
	v_mov_b32_e32 v148, v139
	v_mov_b32_e32 v147, v132
	v_mov_b32_e32 v151, v133
	v_mov_b32_e32 v178, v134
	v_mov_b32_e32 v156, v135
	v_add_u32_e32 v132, v198, v197
	s_movk_i32 s0, 0x300
	v_mul_lo_u32 v132, v132, s0
	v_sub_u32_e32 v132, v194, v132
	v_cndmask_b32_e64 v134, v199, v132, s[44:45]
	v_lshrrev_b32_e32 v132, 7, v134
	v_mad_u64_u32 v[132:133], s[0:1], v195, s13, v[132:133]
	v_lshlrev_b32_e32 v133, 4, v134
	v_lshl_add_u32 v132, v132, 19, v196
	v_and_b32_e32 v133, 0x600, v133
	v_and_b32_e32 v134, 31, v134
	v_or3_b32 v134, v132, v133, v134
	v_add_u32_e32 v132, 0xfffff280, v193
	v_mul_hi_i32 v133, v132, s6
	v_lshrrev_b32_e32 v135, 31, v133
	v_ashrrev_i32_e32 v133, 6, v133
	v_add_u32_e32 v133, v133, v135
	v_mul_i32_i24_e32 v135, 0x180, v133
	v_sub_u32_e32 v132, v132, v135
	v_mul_i32_i24_e32 v135, 0x2aab, v132
	v_lshrrev_b32_e32 v136, 31, v135
	v_ashrrev_i32_e32 v135, 20, v135
	v_add_u16_e32 v135, v135, v136
	v_mul_lo_u16_e32 v136, 0x60, v135
	v_sub_u16_e32 v132, v132, v136
	v_bfe_i32 v136, v132, 0, 16
	v_mul_i32_i24_e32 v132, 0x600000, v133
	v_and_or_b32 v132, v136, 31, v132
	v_add_u32_e32 v133, s5, v135
	s_mov_b32 s0, 0x60000
	v_lshlrev_b32_e32 v135, 4, v136
	v_mad_u64_u32 v[132:133], s[0:1], v133, s0, v[132:133]
	v_and_b32_e32 v135, 0xfffffe00, v135
	s_mov_b32 s0, 0x3800000
	v_add3_u32 v135, v132, v135, s0
	v_add_u32_e32 v132, 0xffffef80, v193
	v_mul_hi_i32 v133, v132, s6
	v_lshrrev_b32_e32 v136, 31, v133
	v_ashrrev_i32_e32 v133, 7, v133
	v_add_u32_e32 v133, v133, v136
	v_mul_i32_i24_e32 v136, 0x300, v133
	v_sub_u32_e32 v132, v132, v136
	v_mul_i32_i24_e32 v136, 0x2aab, v132
	v_lshrrev_b32_e32 v137, 31, v136
	v_ashrrev_i32_e32 v136, 21, v136
	v_add_u16_e32 v136, v136, v137
	v_mul_lo_u16_e32 v137, 0xc0, v136
	v_sub_u16_e32 v132, v132, v137
	s_mov_b32 s0, 0xc00000
	v_bfe_i32 v137, v132, 0, 16
	v_mul_lo_u32 v132, v133, s0
	v_and_or_b32 v132, v137, 31, v132
	v_add_u32_e32 v133, s5, v136
	s_mov_b32 s0, 0xc0000
	v_lshlrev_b32_e32 v136, 4, v137
	v_mad_u64_u32 v[132:133], s[0:1], v133, s0, v[132:133]
	v_and_b32_e32 v136, 0xfffffe00, v136
	s_mov_b32 s0, 0x4400000
	v_add3_u32 v132, v132, v136, s0
	s_movk_i32 s0, 0xd80
	v_cmp_gt_i32_e32 vcc, s0, v193
	s_movk_i32 s0, 0x1710
	v_cmp_gt_u32_e64 s[44:45], s0, v194
	s_movk_i32 s0, 0x1680
	v_add_u32_e32 v133, s2, v194
	v_cndmask_b32_e64 v137, 0, v237, s[44:45]
	v_cmp_gt_i32_e64 s[46:47], s0, v193
	s_movk_i32 s0, 0x1080
	v_cndmask_b32_e32 v136, v236, v218, vcc
	v_cndmask_b32_e64 v137, v137, v239, s[46:47]
	v_cmp_gt_i32_e64 s[44:45], s0, v193
	v_cndmask_b32_e64 v132, v133, v132, s[46:47]
	s_nop 0
	v_cndmask_b32_e64 v158, v137, v136, s[44:45]
	v_cndmask_b32_e64 v132, v132, v135, s[44:45]
	v_cndmask_b32_e32 v172, v132, v134, vcc
	v_cvt_pk_bf16_f32 v132, v144, v145
	v_cmp_ne_u32_e64 s[44:45], 0, v158
	v_cndmask_b32_e64 v145, 4, 5, s[46:47]
	v_cvt_pk_bf16_f32 v133, v146, v148
	v_cvt_pk_bf16_f32 v134, v147, v151
	v_cvt_pk_bf16_f32 v135, v178, v156
	s_and_saveexec_b64 s[0:1], s[44:45]
	v_mul_u32_u24_e32 v136, s4, v158
	v_lshl_or_b32 v136, v192, v145, v136
	v_add_u32_e32 v212, v136, v172
	v_lshl_add_u64 v[136:137], v[212:213], 1, s[52:53]
	global_store_dwordx4 v[136:137], v[132:135], off nt
	s_nop 1
	s_or_b64 exec, exec, s[0:1]
	v_mul_f32_e32 v134, 0xbfb8aa3b, v128
	v_exp_f32_e32 v134, v134
	s_nop 0
	v_add_f32_e32 v134, 1.0, v134
	v_rcp_f32_e32 v146, v134
	v_mul_f32_e32 v134, 0xbfb8aa3b, v124
	v_exp_f32_e32 v134, v134
	s_nop 0
	v_add_f32_e32 v134, 1.0, v134
	v_rcp_f32_e32 v148, v134
	v_mul_f32_e32 v134, 0xbfb8aa3b, v129
	v_exp_f32_e32 v134, v134
	s_nop 0
	v_add_f32_e32 v134, 1.0, v134
	v_rcp_f32_e32 v147, v134
	v_mul_f32_e32 v134, 0xbfb8aa3b, v125
	v_exp_f32_e32 v134, v134
	v_pk_mul_f32 v[128:129], v[128:129], v[146:147]
	v_add_f32_e32 v134, 1.0, v134
	v_rcp_f32_e32 v149, v134
	v_mul_f32_e32 v134, 0xbfb8aa3b, v130
	v_exp_f32_e32 v134, v134
	v_pk_mul_f32 v[124:125], v[124:125], v[148:149]
	v_add_f32_e32 v134, 1.0, v134
	v_rcp_f32_e32 v150, v134
	v_mul_f32_e32 v134, 0xbfb8aa3b, v126
	v_exp_f32_e32 v134, v134
	s_nop 0
	v_add_f32_e32 v134, 1.0, v134
	v_rcp_f32_e32 v152, v134
	v_mul_f32_e32 v134, 0xbfb8aa3b, v131
	v_exp_f32_e32 v134, v134
	s_nop 0
	v_add_f32_e32 v134, 1.0, v134
	v_rcp_f32_e32 v151, v134
	v_mul_f32_e32 v134, 0xbfb8aa3b, v127
	v_exp_f32_e32 v134, v134
	v_pk_mul_f32 v[130:131], v[130:131], v[150:151]
	v_add_f32_e32 v134, 1.0, v134
	v_rcp_f32_e32 v153, v134
	s_nop 0
	v_pk_mul_f32 v[126:127], v[126:127], v[152:153]
	s_or_b32 s2, s4, 1
	v_cvt_pk_bf16_f32 v127, v126, v127
	v_cvt_pk_bf16_f32 v126, v124, v125
	v_cvt_pk_bf16_f32 v124, v128, v129
	v_cvt_pk_bf16_f32 v125, v130, v131
	s_and_saveexec_b64 s[0:1], s[42:43]
	v_mul_u32_u24_e32 v128, s2, v159
	v_lshlrev_b32_e32 v129, v180, v192
	v_add3_u32 v212, v128, v129, v181
	v_lshl_add_u64 v[128:129], v[212:213], 1, s[52:53]
	global_store_dwordx4 v[128:129], v[124:127], off nt
	s_nop 1
	s_or_b64 exec, exec, s[0:1]
	v_mul_f32_e32 v125, 0xbfb8aa3b, v112
	v_exp_f32_e32 v125, v125
	v_mul_f32_e32 v124, 0xbfb8aa3b, v116
	v_exp_f32_e32 v124, v124
	v_mul_f32_e32 v129, 0xbfb8aa3b, v114
	v_add_f32_e32 v125, 1.0, v125
	v_rcp_f32_e32 v126, v125
	v_mul_f32_e32 v125, 0xbfb8aa3b, v117
	v_exp_f32_e32 v125, v125
	v_add_f32_e32 v124, 1.0, v124
	v_exp_f32_e32 v129, v129
	v_rcp_f32_e32 v124, v124
	v_add_f32_e32 v125, 1.0, v125
	v_rcp_f32_e32 v125, v125
	v_add_f32_e32 v129, 1.0, v129
	v_mul_f32_e32 v127, 0xbfb8aa3b, v113
	v_mul_f32_e32 v128, 0xbfb8aa3b, v118
	v_rcp_f32_e32 v130, v129
	v_mul_f32_e32 v129, 0xbfb8aa3b, v119
	v_pk_mul_f32 v[116:117], v[116:117], v[124:125]
	v_mul_f32_e32 v124, 0xbfb8aa3b, v115
	v_exp_f32_e32 v127, v127
	v_exp_f32_e32 v128, v128
	v_exp_f32_e32 v129, v129
	v_exp_f32_e32 v124, v124
	v_add_f32_e32 v127, 1.0, v127
	v_add_f32_e32 v128, 1.0, v128
	v_add_f32_e32 v129, 1.0, v129
	v_add_f32_e32 v124, 1.0, v124
	v_rcp_f32_e32 v127, v127
	v_rcp_f32_e32 v128, v128
	v_rcp_f32_e32 v129, v129
	v_rcp_f32_e32 v131, v124
	v_pk_mul_f32 v[112:113], v[112:113], v[126:127]
	v_pk_mul_f32 v[118:119], v[118:119], v[128:129]
	v_pk_mul_f32 v[114:115], v[114:115], v[130:131]
	v_cvt_pk_bf16_f32 v115, v114, v115
	v_cvt_pk_bf16_f32 v114, v112, v113
	v_cvt_pk_bf16_f32 v112, v116, v117
	v_cvt_pk_bf16_f32 v113, v118, v119
	s_and_saveexec_b64 s[0:1], s[44:45]
	v_mul_u32_u24_e32 v116, s2, v158
	v_lshlrev_b32_e32 v117, v145, v192
	v_add3_u32 v212, v116, v117, v172
	v_lshl_add_u64 v[116:117], v[212:213], 1, s[52:53]
	global_store_dwordx4 v[116:117], v[112:115], off nt
	s_nop 1
	s_or_b64 exec, exec, s[0:1]
	v_mul_f32_e32 v114, 0xbfb8aa3b, v108
	v_exp_f32_e32 v114, v114
	s_nop 0
	v_add_f32_e32 v114, 1.0, v114
	v_rcp_f32_e32 v126, v114
	v_mul_f32_e32 v114, 0xbfb8aa3b, v104
	v_exp_f32_e32 v114, v114
	s_nop 0
	v_add_f32_e32 v114, 1.0, v114
	v_rcp_f32_e32 v128, v114
	v_mul_f32_e32 v114, 0xbfb8aa3b, v109
	v_exp_f32_e32 v114, v114
	s_nop 0
	v_add_f32_e32 v114, 1.0, v114
	v_rcp_f32_e32 v127, v114
	v_mul_f32_e32 v114, 0xbfb8aa3b, v105
	v_exp_f32_e32 v114, v114
	v_pk_mul_f32 v[108:109], v[108:109], v[126:127]
	v_add_f32_e32 v114, 1.0, v114
	v_rcp_f32_e32 v129, v114
	v_mul_f32_e32 v114, 0xbfb8aa3b, v110
	v_exp_f32_e32 v114, v114
	v_pk_mul_f32 v[104:105], v[104:105], v[128:129]
	v_add_f32_e32 v114, 1.0, v114
	v_rcp_f32_e32 v130, v114
	v_mul_f32_e32 v114, 0xbfb8aa3b, v106
	v_exp_f32_e32 v114, v114
	s_nop 0
	v_add_f32_e32 v114, 1.0, v114
	v_rcp_f32_e32 v132, v114
	v_mul_f32_e32 v114, 0xbfb8aa3b, v111
	v_exp_f32_e32 v114, v114
	s_nop 0
	v_add_f32_e32 v114, 1.0, v114
	v_rcp_f32_e32 v131, v114
	v_mul_f32_e32 v114, 0xbfb8aa3b, v107
	v_exp_f32_e32 v114, v114
	v_pk_mul_f32 v[110:111], v[110:111], v[130:131]
	v_add_f32_e32 v114, 1.0, v114
	v_rcp_f32_e32 v133, v114
	s_nop 0
	v_pk_mul_f32 v[106:107], v[106:107], v[132:133]
	s_or_b32 s2, s4, 2
	v_cvt_pk_bf16_f32 v107, v106, v107
	v_cvt_pk_bf16_f32 v106, v104, v105
	v_cvt_pk_bf16_f32 v104, v108, v109
	v_cvt_pk_bf16_f32 v105, v110, v111
	s_and_saveexec_b64 s[0:1], s[42:43]
	v_mul_u32_u24_e32 v108, s2, v159
	v_lshl_or_b32 v108, v192, v180, v108
	v_add_u32_e32 v212, v108, v181
	v_lshl_add_u64 v[108:109], v[212:213], 1, s[52:53]
	global_store_dwordx4 v[108:109], v[104:107], off nt
	s_nop 1
	s_or_b64 exec, exec, s[0:1]
	v_mul_f32_e32 v105, 0xbfb8aa3b, v92
	v_exp_f32_e32 v105, v105
	v_mul_f32_e32 v104, 0xbfb8aa3b, v96
	v_exp_f32_e32 v104, v104
	v_mul_f32_e32 v109, 0xbfb8aa3b, v94
	v_add_f32_e32 v105, 1.0, v105
	v_rcp_f32_e32 v106, v105
	v_mul_f32_e32 v105, 0xbfb8aa3b, v97
	v_exp_f32_e32 v105, v105
	v_add_f32_e32 v104, 1.0, v104
	v_exp_f32_e32 v109, v109
	v_rcp_f32_e32 v104, v104
	v_add_f32_e32 v105, 1.0, v105
	v_rcp_f32_e32 v105, v105
	v_add_f32_e32 v109, 1.0, v109
	v_mul_f32_e32 v107, 0xbfb8aa3b, v93
	v_mul_f32_e32 v108, 0xbfb8aa3b, v98
	v_rcp_f32_e32 v110, v109
	v_mul_f32_e32 v109, 0xbfb8aa3b, v99
	v_pk_mul_f32 v[96:97], v[96:97], v[104:105]
	v_mul_f32_e32 v104, 0xbfb8aa3b, v95
	v_exp_f32_e32 v107, v107
	v_exp_f32_e32 v108, v108
	v_exp_f32_e32 v109, v109
	v_exp_f32_e32 v104, v104
	v_add_f32_e32 v107, 1.0, v107
	v_add_f32_e32 v108, 1.0, v108
	v_add_f32_e32 v109, 1.0, v109
	v_add_f32_e32 v104, 1.0, v104
	v_rcp_f32_e32 v107, v107
	v_rcp_f32_e32 v108, v108
	v_rcp_f32_e32 v109, v109
	v_rcp_f32_e32 v111, v104
	v_pk_mul_f32 v[92:93], v[92:93], v[106:107]
	v_pk_mul_f32 v[98:99], v[98:99], v[108:109]
	v_pk_mul_f32 v[94:95], v[94:95], v[110:111]
	v_cvt_pk_bf16_f32 v95, v94, v95
	v_cvt_pk_bf16_f32 v94, v92, v93
	v_cvt_pk_bf16_f32 v92, v96, v97
	v_cvt_pk_bf16_f32 v93, v98, v99
	s_and_saveexec_b64 s[0:1], s[44:45]
	v_mul_u32_u24_e32 v96, s2, v158
	v_lshl_or_b32 v96, v192, v145, v96
	v_add_u32_e32 v212, v96, v172
	v_lshl_add_u64 v[96:97], v[212:213], 1, s[52:53]
	global_store_dwordx4 v[96:97], v[92:95], off nt
	s_nop 1
	s_or_b64 exec, exec, s[0:1]
	v_mul_f32_e32 v94, 0xbfb8aa3b, v88
	v_exp_f32_e32 v94, v94
	s_nop 0
	v_add_f32_e32 v94, 1.0, v94
	v_rcp_f32_e32 v106, v94
	v_mul_f32_e32 v94, 0xbfb8aa3b, v84
	v_exp_f32_e32 v94, v94
	s_nop 0
	v_add_f32_e32 v94, 1.0, v94
	v_rcp_f32_e32 v108, v94
	v_mul_f32_e32 v94, 0xbfb8aa3b, v89
	v_exp_f32_e32 v94, v94
	s_nop 0
	v_add_f32_e32 v94, 1.0, v94
	v_rcp_f32_e32 v107, v94
	v_mul_f32_e32 v94, 0xbfb8aa3b, v85
	v_exp_f32_e32 v94, v94
	v_pk_mul_f32 v[88:89], v[88:89], v[106:107]
	v_add_f32_e32 v94, 1.0, v94
	v_rcp_f32_e32 v109, v94
	v_mul_f32_e32 v94, 0xbfb8aa3b, v90
	v_exp_f32_e32 v94, v94
	v_pk_mul_f32 v[84:85], v[84:85], v[108:109]
	v_add_f32_e32 v94, 1.0, v94
	v_rcp_f32_e32 v110, v94
	v_mul_f32_e32 v94, 0xbfb8aa3b, v86
	v_exp_f32_e32 v94, v94
	s_nop 0
	v_add_f32_e32 v94, 1.0, v94
	v_rcp_f32_e32 v112, v94
	v_mul_f32_e32 v94, 0xbfb8aa3b, v91
	v_exp_f32_e32 v94, v94
	s_nop 0
	v_add_f32_e32 v94, 1.0, v94
	v_rcp_f32_e32 v111, v94
	v_mul_f32_e32 v94, 0xbfb8aa3b, v87
	v_exp_f32_e32 v94, v94
	v_pk_mul_f32 v[90:91], v[90:91], v[110:111]
	v_add_f32_e32 v94, 1.0, v94
	v_rcp_f32_e32 v113, v94
	s_nop 0
	v_pk_mul_f32 v[86:87], v[86:87], v[112:113]
	s_or_b32 s2, s4, 3
	v_cvt_pk_bf16_f32 v87, v86, v87
	v_cvt_pk_bf16_f32 v86, v84, v85
	v_cvt_pk_bf16_f32 v84, v88, v89
	v_cvt_pk_bf16_f32 v85, v90, v91
	s_and_saveexec_b64 s[0:1], s[42:43]
	v_mul_u32_u24_e32 v88, s2, v159
	v_lshlrev_b32_e32 v89, v180, v192
	v_add3_u32 v212, v88, v89, v181
	v_lshl_add_u64 v[88:89], v[212:213], 1, s[52:53]
	global_store_dwordx4 v[88:89], v[84:87], off nt
	s_nop 1
	s_or_b64 exec, exec, s[0:1]
	v_mul_f32_e32 v85, 0xbfb8aa3b, v72
	v_exp_f32_e32 v85, v85
	v_mul_f32_e32 v84, 0xbfb8aa3b, v76
	v_exp_f32_e32 v84, v84
	v_mul_f32_e32 v89, 0xbfb8aa3b, v74
	v_add_f32_e32 v85, 1.0, v85
	v_rcp_f32_e32 v86, v85
	v_mul_f32_e32 v85, 0xbfb8aa3b, v77
	v_exp_f32_e32 v85, v85
	v_add_f32_e32 v84, 1.0, v84
	v_exp_f32_e32 v89, v89
	v_rcp_f32_e32 v84, v84
	v_add_f32_e32 v85, 1.0, v85
	v_rcp_f32_e32 v85, v85
	v_add_f32_e32 v89, 1.0, v89
	v_mul_f32_e32 v87, 0xbfb8aa3b, v73
	v_mul_f32_e32 v88, 0xbfb8aa3b, v78
	v_rcp_f32_e32 v90, v89
	v_mul_f32_e32 v89, 0xbfb8aa3b, v79
	v_pk_mul_f32 v[76:77], v[76:77], v[84:85]
	v_mul_f32_e32 v84, 0xbfb8aa3b, v75
	v_exp_f32_e32 v87, v87
	v_exp_f32_e32 v88, v88
	v_exp_f32_e32 v89, v89
	v_exp_f32_e32 v84, v84
	v_add_f32_e32 v87, 1.0, v87
	v_add_f32_e32 v88, 1.0, v88
	v_add_f32_e32 v89, 1.0, v89
	v_add_f32_e32 v84, 1.0, v84
	v_rcp_f32_e32 v87, v87
	v_rcp_f32_e32 v88, v88
	v_rcp_f32_e32 v89, v89
	v_rcp_f32_e32 v91, v84
	v_pk_mul_f32 v[72:73], v[72:73], v[86:87]
	v_pk_mul_f32 v[78:79], v[78:79], v[88:89]
	v_pk_mul_f32 v[74:75], v[74:75], v[90:91]
	v_cvt_pk_bf16_f32 v75, v74, v75
	v_cvt_pk_bf16_f32 v74, v72, v73
	v_cvt_pk_bf16_f32 v72, v76, v77
	v_cvt_pk_bf16_f32 v73, v78, v79
	s_and_saveexec_b64 s[0:1], s[44:45]
	v_mul_u32_u24_e32 v76, s2, v158
	v_lshlrev_b32_e32 v77, v145, v192
	v_add3_u32 v212, v76, v77, v172
	v_lshl_add_u64 v[76:77], v[212:213], 1, s[52:53]
	global_store_dwordx4 v[76:77], v[72:75], off nt
	s_nop 1
	s_or_b64 exec, exec, s[0:1]
	s_mov_b64 s[0:1], -1
	v_mul_f32_e32 v74, 0xbfb8aa3b, v68
	v_exp_f32_e32 v74, v74
	s_nop 0
	v_add_f32_e32 v74, 1.0, v74
	v_rcp_f32_e32 v86, v74
	v_mul_f32_e32 v74, 0xbfb8aa3b, v64
	v_exp_f32_e32 v74, v74
	s_nop 0
	v_add_f32_e32 v74, 1.0, v74
	v_rcp_f32_e32 v88, v74
	v_mul_f32_e32 v74, 0xbfb8aa3b, v69
	v_exp_f32_e32 v74, v74
	s_nop 0
	v_add_f32_e32 v74, 1.0, v74
	v_rcp_f32_e32 v87, v74
	v_mul_f32_e32 v74, 0xbfb8aa3b, v65
	v_exp_f32_e32 v74, v74
	v_pk_mul_f32 v[68:69], v[68:69], v[86:87]
	v_add_f32_e32 v74, 1.0, v74
	v_rcp_f32_e32 v89, v74
	v_mul_f32_e32 v74, 0xbfb8aa3b, v70
	v_exp_f32_e32 v74, v74
	v_pk_mul_f32 v[64:65], v[64:65], v[88:89]
	v_add_f32_e32 v74, 1.0, v74
	v_rcp_f32_e32 v90, v74
	v_mul_f32_e32 v74, 0xbfb8aa3b, v66
	v_exp_f32_e32 v74, v74
	s_nop 0
	v_add_f32_e32 v74, 1.0, v74
	v_rcp_f32_e32 v92, v74
	v_mul_f32_e32 v74, 0xbfb8aa3b, v71
	v_exp_f32_e32 v74, v74
	s_nop 0
	v_add_f32_e32 v74, 1.0, v74
	v_rcp_f32_e32 v91, v74
	v_mul_f32_e32 v74, 0xbfb8aa3b, v67
	v_exp_f32_e32 v74, v74
	v_pk_mul_f32 v[70:71], v[70:71], v[90:91]
	v_add_f32_e32 v74, 1.0, v74
	v_rcp_f32_e32 v93, v74
	s_nop 0
	v_pk_mul_f32 v[66:67], v[66:67], v[92:93]
	s_addk_i32 s8, 0x80
	s_lshr_b32 s0, s8, 4
	s_and_b32 s2, s0, 0xfc
	v_cvt_pk_bf16_f32 v67, v66, v67
	v_cvt_pk_bf16_f32 v66, v64, v65
	v_cvt_pk_bf16_f32 v64, v68, v69
	v_cvt_pk_bf16_f32 v65, v70, v71
	s_and_saveexec_b64 s[0:1], s[42:43]
	v_mul_u32_u24_e32 v68, s2, v159
	v_lshl_or_b32 v68, v192, v180, v68
	v_add_u32_e32 v212, v68, v181
	v_lshl_add_u64 v[68:69], v[212:213], 1, s[52:53]
	global_store_dwordx4 v[68:69], v[64:67], off nt
	s_nop 1
	s_or_b64 exec, exec, s[0:1]
	v_mul_f32_e32 v65, 0xbfb8aa3b, v52
	v_exp_f32_e32 v65, v65
	v_mul_f32_e32 v64, 0xbfb8aa3b, v56
	v_exp_f32_e32 v64, v64
	v_mul_f32_e32 v69, 0xbfb8aa3b, v54
	v_add_f32_e32 v65, 1.0, v65
	v_rcp_f32_e32 v66, v65
	v_mul_f32_e32 v65, 0xbfb8aa3b, v57
	v_exp_f32_e32 v65, v65
	v_add_f32_e32 v64, 1.0, v64
	v_exp_f32_e32 v69, v69
	v_rcp_f32_e32 v64, v64
	v_add_f32_e32 v65, 1.0, v65
	v_rcp_f32_e32 v65, v65
	v_add_f32_e32 v69, 1.0, v69
	v_mul_f32_e32 v67, 0xbfb8aa3b, v53
	v_mul_f32_e32 v68, 0xbfb8aa3b, v58
	v_rcp_f32_e32 v70, v69
	v_mul_f32_e32 v69, 0xbfb8aa3b, v59
	v_pk_mul_f32 v[56:57], v[56:57], v[64:65]
	v_mul_f32_e32 v64, 0xbfb8aa3b, v55
	v_exp_f32_e32 v67, v67
	v_exp_f32_e32 v68, v68
	v_exp_f32_e32 v69, v69
	v_exp_f32_e32 v64, v64
	v_add_f32_e32 v67, 1.0, v67
	v_add_f32_e32 v68, 1.0, v68
	v_add_f32_e32 v69, 1.0, v69
	v_add_f32_e32 v64, 1.0, v64
	v_rcp_f32_e32 v67, v67
	v_rcp_f32_e32 v68, v68
	v_rcp_f32_e32 v69, v69
	v_rcp_f32_e32 v71, v64
	v_pk_mul_f32 v[52:53], v[52:53], v[66:67]
	v_pk_mul_f32 v[58:59], v[58:59], v[68:69]
	v_pk_mul_f32 v[54:55], v[54:55], v[70:71]
	v_cvt_pk_bf16_f32 v55, v54, v55
	v_cvt_pk_bf16_f32 v54, v52, v53
	v_cvt_pk_bf16_f32 v52, v56, v57
	v_cvt_pk_bf16_f32 v53, v58, v59
	s_and_saveexec_b64 s[0:1], s[44:45]
	v_mul_u32_u24_e32 v56, s2, v158
	v_lshl_or_b32 v56, v192, v145, v56
	v_add_u32_e32 v212, v56, v172
	v_lshl_add_u64 v[56:57], v[212:213], 1, s[52:53]
	global_store_dwordx4 v[56:57], v[52:55], off nt
	s_nop 1
	s_or_b64 exec, exec, s[0:1]
	v_mul_f32_e32 v54, 0xbfb8aa3b, v48
	v_exp_f32_e32 v54, v54
	s_nop 0
	v_add_f32_e32 v54, 1.0, v54
	v_rcp_f32_e32 v66, v54
	v_mul_f32_e32 v54, 0xbfb8aa3b, v44
	v_exp_f32_e32 v54, v54
	s_nop 0
	v_add_f32_e32 v54, 1.0, v54
	v_rcp_f32_e32 v68, v54
	v_mul_f32_e32 v54, 0xbfb8aa3b, v49
	v_exp_f32_e32 v54, v54
	s_nop 0
	v_add_f32_e32 v54, 1.0, v54
	v_rcp_f32_e32 v67, v54
	v_mul_f32_e32 v54, 0xbfb8aa3b, v45
	v_exp_f32_e32 v54, v54
	v_pk_mul_f32 v[48:49], v[48:49], v[66:67]
	v_add_f32_e32 v54, 1.0, v54
	v_rcp_f32_e32 v69, v54
	v_mul_f32_e32 v54, 0xbfb8aa3b, v50
	v_exp_f32_e32 v54, v54
	v_pk_mul_f32 v[44:45], v[44:45], v[68:69]
	v_add_f32_e32 v54, 1.0, v54
	v_rcp_f32_e32 v70, v54
	v_mul_f32_e32 v54, 0xbfb8aa3b, v46
	v_exp_f32_e32 v54, v54
	s_nop 0
	v_add_f32_e32 v54, 1.0, v54
	v_rcp_f32_e32 v72, v54
	v_mul_f32_e32 v54, 0xbfb8aa3b, v51
	v_exp_f32_e32 v54, v54
	s_nop 0
	v_add_f32_e32 v54, 1.0, v54
	v_rcp_f32_e32 v71, v54
	v_mul_f32_e32 v54, 0xbfb8aa3b, v47
	v_exp_f32_e32 v54, v54
	v_pk_mul_f32 v[50:51], v[50:51], v[70:71]
	v_add_f32_e32 v54, 1.0, v54
	v_rcp_f32_e32 v73, v54
	s_nop 0
	v_pk_mul_f32 v[46:47], v[46:47], v[72:73]
	s_or_b32 s4, s2, 1
	v_cvt_pk_bf16_f32 v47, v46, v47
	v_cvt_pk_bf16_f32 v46, v44, v45
	v_cvt_pk_bf16_f32 v44, v48, v49
	v_cvt_pk_bf16_f32 v45, v50, v51
	s_and_saveexec_b64 s[0:1], s[42:43]
	v_mul_u32_u24_e32 v48, s4, v159
	v_lshlrev_b32_e32 v49, v180, v192
	v_add3_u32 v212, v48, v49, v181
	v_lshl_add_u64 v[48:49], v[212:213], 1, s[52:53]
	global_store_dwordx4 v[48:49], v[44:47], off nt
	s_nop 1
	s_or_b64 exec, exec, s[0:1]
	v_mul_f32_e32 v45, 0xbfb8aa3b, v32
	v_exp_f32_e32 v45, v45
	v_mul_f32_e32 v44, 0xbfb8aa3b, v36
	v_exp_f32_e32 v44, v44
	v_mul_f32_e32 v49, 0xbfb8aa3b, v34
	v_add_f32_e32 v45, 1.0, v45
	v_rcp_f32_e32 v46, v45
	v_mul_f32_e32 v45, 0xbfb8aa3b, v37
	v_exp_f32_e32 v45, v45
	v_add_f32_e32 v44, 1.0, v44
	v_exp_f32_e32 v49, v49
	v_rcp_f32_e32 v44, v44
	v_add_f32_e32 v45, 1.0, v45
	v_rcp_f32_e32 v45, v45
	v_add_f32_e32 v49, 1.0, v49
	v_mul_f32_e32 v47, 0xbfb8aa3b, v33
	v_mul_f32_e32 v48, 0xbfb8aa3b, v38
	v_rcp_f32_e32 v50, v49
	v_mul_f32_e32 v49, 0xbfb8aa3b, v39
	v_pk_mul_f32 v[36:37], v[36:37], v[44:45]
	v_mul_f32_e32 v44, 0xbfb8aa3b, v35
	v_exp_f32_e32 v47, v47
	v_exp_f32_e32 v48, v48
	v_exp_f32_e32 v49, v49
	v_exp_f32_e32 v44, v44
	v_add_f32_e32 v47, 1.0, v47
	v_add_f32_e32 v48, 1.0, v48
	v_add_f32_e32 v49, 1.0, v49
	v_add_f32_e32 v44, 1.0, v44
	v_rcp_f32_e32 v47, v47
	v_rcp_f32_e32 v48, v48
	v_rcp_f32_e32 v49, v49
	v_rcp_f32_e32 v51, v44
	v_pk_mul_f32 v[32:33], v[32:33], v[46:47]
	v_pk_mul_f32 v[38:39], v[38:39], v[48:49]
	v_pk_mul_f32 v[34:35], v[34:35], v[50:51]
	v_cvt_pk_bf16_f32 v35, v34, v35
	v_cvt_pk_bf16_f32 v34, v32, v33
	v_cvt_pk_bf16_f32 v32, v36, v37
	v_cvt_pk_bf16_f32 v33, v38, v39
	s_and_saveexec_b64 s[0:1], s[44:45]
	v_mul_u32_u24_e32 v36, s4, v158
	v_lshlrev_b32_e32 v37, v145, v192
	v_add3_u32 v212, v36, v37, v172
	v_lshl_add_u64 v[36:37], v[212:213], 1, s[52:53]
	global_store_dwordx4 v[36:37], v[32:35], off nt
	s_nop 1
	s_or_b64 exec, exec, s[0:1]
	v_mul_f32_e32 v34, 0xbfb8aa3b, v28
	v_exp_f32_e32 v34, v34
	s_nop 0
	v_add_f32_e32 v34, 1.0, v34
	v_rcp_f32_e32 v46, v34
	v_mul_f32_e32 v34, 0xbfb8aa3b, v24
	v_exp_f32_e32 v34, v34
	s_nop 0
	v_add_f32_e32 v34, 1.0, v34
	v_rcp_f32_e32 v48, v34
	v_mul_f32_e32 v34, 0xbfb8aa3b, v29
	v_exp_f32_e32 v34, v34
	s_nop 0
	v_add_f32_e32 v34, 1.0, v34
	v_rcp_f32_e32 v47, v34
	v_mul_f32_e32 v34, 0xbfb8aa3b, v25
	v_exp_f32_e32 v34, v34
	v_pk_mul_f32 v[28:29], v[28:29], v[46:47]
	v_add_f32_e32 v34, 1.0, v34
	v_rcp_f32_e32 v49, v34
	v_mul_f32_e32 v34, 0xbfb8aa3b, v30
	v_exp_f32_e32 v34, v34
	v_pk_mul_f32 v[24:25], v[24:25], v[48:49]
	v_add_f32_e32 v34, 1.0, v34
	v_rcp_f32_e32 v50, v34
	v_mul_f32_e32 v34, 0xbfb8aa3b, v26
	v_exp_f32_e32 v34, v34
	s_nop 0
	v_add_f32_e32 v34, 1.0, v34
	v_rcp_f32_e32 v52, v34
	v_mul_f32_e32 v34, 0xbfb8aa3b, v31
	v_exp_f32_e32 v34, v34
	s_nop 0
	v_add_f32_e32 v34, 1.0, v34
	v_rcp_f32_e32 v51, v34
	v_mul_f32_e32 v34, 0xbfb8aa3b, v27
	v_exp_f32_e32 v34, v34
	v_pk_mul_f32 v[30:31], v[30:31], v[50:51]
	v_add_f32_e32 v34, 1.0, v34
	v_rcp_f32_e32 v53, v34
	s_nop 0
	v_pk_mul_f32 v[26:27], v[26:27], v[52:53]
	s_or_b32 s4, s2, 2
	v_cvt_pk_bf16_f32 v27, v26, v27
	v_cvt_pk_bf16_f32 v26, v24, v25
	v_cvt_pk_bf16_f32 v24, v28, v29
	v_cvt_pk_bf16_f32 v25, v30, v31
	s_and_saveexec_b64 s[0:1], s[42:43]
	v_mul_u32_u24_e32 v28, s4, v159
	v_lshl_or_b32 v28, v192, v180, v28
	v_add_u32_e32 v212, v28, v181
	v_lshl_add_u64 v[28:29], v[212:213], 1, s[52:53]
	global_store_dwordx4 v[28:29], v[24:27], off nt
	s_nop 1
	s_or_b64 exec, exec, s[0:1]
	v_mul_f32_e32 v25, 0xbfb8aa3b, v16
	v_exp_f32_e32 v25, v25
	v_mul_f32_e32 v24, 0xbfb8aa3b, v20
	v_exp_f32_e32 v24, v24
	v_mul_f32_e32 v29, 0xbfb8aa3b, v18
	v_add_f32_e32 v25, 1.0, v25
	v_rcp_f32_e32 v26, v25
	v_mul_f32_e32 v25, 0xbfb8aa3b, v21
	v_exp_f32_e32 v25, v25
	v_add_f32_e32 v24, 1.0, v24
	v_exp_f32_e32 v29, v29
	v_rcp_f32_e32 v24, v24
	v_add_f32_e32 v25, 1.0, v25
	v_rcp_f32_e32 v25, v25
	v_add_f32_e32 v29, 1.0, v29
	v_mul_f32_e32 v27, 0xbfb8aa3b, v17
	v_mul_f32_e32 v28, 0xbfb8aa3b, v22
	v_rcp_f32_e32 v30, v29
	v_mul_f32_e32 v29, 0xbfb8aa3b, v23
	v_pk_mul_f32 v[20:21], v[20:21], v[24:25]
	v_mul_f32_e32 v24, 0xbfb8aa3b, v19
	v_exp_f32_e32 v27, v27
	v_exp_f32_e32 v28, v28
	v_exp_f32_e32 v29, v29
	v_exp_f32_e32 v24, v24
	v_add_f32_e32 v27, 1.0, v27
	v_add_f32_e32 v28, 1.0, v28
	v_add_f32_e32 v29, 1.0, v29
	v_add_f32_e32 v24, 1.0, v24
	v_rcp_f32_e32 v27, v27
	v_rcp_f32_e32 v28, v28
	v_rcp_f32_e32 v29, v29
	v_rcp_f32_e32 v31, v24
	v_pk_mul_f32 v[16:17], v[16:17], v[26:27]
	v_pk_mul_f32 v[22:23], v[22:23], v[28:29]
	v_pk_mul_f32 v[18:19], v[18:19], v[30:31]
	v_cvt_pk_bf16_f32 v19, v18, v19
	v_cvt_pk_bf16_f32 v18, v16, v17
	v_cvt_pk_bf16_f32 v16, v20, v21
	v_cvt_pk_bf16_f32 v17, v22, v23
	s_and_saveexec_b64 s[0:1], s[44:45]
	v_mul_u32_u24_e32 v20, s4, v158
	v_lshl_or_b32 v20, v192, v145, v20
	v_add_u32_e32 v212, v20, v172
	v_lshl_add_u64 v[20:21], v[212:213], 1, s[52:53]
	global_store_dwordx4 v[20:21], v[16:19], off nt
	s_nop 1
	s_or_b64 exec, exec, s[0:1]
	v_mul_f32_e32 v18, 0xbfb8aa3b, v12
	v_exp_f32_e32 v18, v18
	s_nop 0
	v_add_f32_e32 v18, 1.0, v18
	v_rcp_f32_e32 v26, v18
	v_mul_f32_e32 v18, 0xbfb8aa3b, v8
	v_exp_f32_e32 v18, v18
	s_nop 0
	v_add_f32_e32 v18, 1.0, v18
	v_rcp_f32_e32 v28, v18
	v_mul_f32_e32 v18, 0xbfb8aa3b, v13
	v_exp_f32_e32 v18, v18
	s_nop 0
	v_add_f32_e32 v18, 1.0, v18
	v_rcp_f32_e32 v27, v18
	v_mul_f32_e32 v18, 0xbfb8aa3b, v9
	v_exp_f32_e32 v18, v18
	v_pk_mul_f32 v[12:13], v[12:13], v[26:27]
	v_add_f32_e32 v18, 1.0, v18
	v_rcp_f32_e32 v29, v18
	v_mul_f32_e32 v18, 0xbfb8aa3b, v14
	v_exp_f32_e32 v18, v18
	v_pk_mul_f32 v[8:9], v[8:9], v[28:29]
	v_add_f32_e32 v18, 1.0, v18
	v_rcp_f32_e32 v30, v18
	v_mul_f32_e32 v18, 0xbfb8aa3b, v10
	v_exp_f32_e32 v18, v18
	s_nop 0
	v_add_f32_e32 v18, 1.0, v18
	v_rcp_f32_e32 v32, v18
	v_mul_f32_e32 v18, 0xbfb8aa3b, v15
	v_exp_f32_e32 v18, v18
	s_nop 0
	v_add_f32_e32 v18, 1.0, v18
	v_rcp_f32_e32 v31, v18
	v_mul_f32_e32 v18, 0xbfb8aa3b, v11
	v_exp_f32_e32 v18, v18
	v_pk_mul_f32 v[14:15], v[14:15], v[30:31]
	v_add_f32_e32 v18, 1.0, v18
	v_rcp_f32_e32 v33, v18
	s_nop 0
	v_pk_mul_f32 v[10:11], v[10:11], v[32:33]
	s_or_b32 s2, s2, 3
	v_cvt_pk_bf16_f32 v11, v10, v11
	v_cvt_pk_bf16_f32 v10, v8, v9
	v_cvt_pk_bf16_f32 v8, v12, v13
	v_cvt_pk_bf16_f32 v9, v14, v15
	s_and_saveexec_b64 s[0:1], s[42:43]
	v_mul_u32_u24_e32 v12, s2, v159
	v_lshlrev_b32_e32 v13, v180, v192
	v_add3_u32 v212, v12, v13, v181
	v_lshl_add_u64 v[12:13], v[212:213], 1, s[52:53]
	global_store_dwordx4 v[12:13], v[8:11], off nt
	s_nop 1
	s_or_b64 exec, exec, s[0:1]
	s_and_b64 vcc, exec, s[38:39]
	v_mul_f32_e32 v9, 0xbfb8aa3b, v0
	v_exp_f32_e32 v9, v9
	v_mul_f32_e32 v8, 0xbfb8aa3b, v4
	v_exp_f32_e32 v8, v8
	v_mul_f32_e32 v13, 0xbfb8aa3b, v2
	v_add_f32_e32 v9, 1.0, v9
	v_rcp_f32_e32 v10, v9
	v_mul_f32_e32 v9, 0xbfb8aa3b, v5
	v_exp_f32_e32 v9, v9
	v_add_f32_e32 v8, 1.0, v8
	v_exp_f32_e32 v13, v13
	v_rcp_f32_e32 v8, v8
	v_add_f32_e32 v9, 1.0, v9
	v_rcp_f32_e32 v9, v9
	v_add_f32_e32 v13, 1.0, v13
	v_mul_f32_e32 v11, 0xbfb8aa3b, v1
	v_mul_f32_e32 v12, 0xbfb8aa3b, v6
	v_rcp_f32_e32 v14, v13
	v_mul_f32_e32 v13, 0xbfb8aa3b, v7
	v_pk_mul_f32 v[4:5], v[4:5], v[8:9]
	v_mul_f32_e32 v8, 0xbfb8aa3b, v3
	v_exp_f32_e32 v11, v11
	v_exp_f32_e32 v12, v12
	v_exp_f32_e32 v13, v13
	v_exp_f32_e32 v8, v8
	v_add_f32_e32 v11, 1.0, v11
	v_add_f32_e32 v12, 1.0, v12
	v_add_f32_e32 v13, 1.0, v13
	v_add_f32_e32 v8, 1.0, v8
	v_rcp_f32_e32 v11, v11
	v_rcp_f32_e32 v12, v12
	v_rcp_f32_e32 v13, v13
	v_rcp_f32_e32 v15, v8
	v_pk_mul_f32 v[0:1], v[0:1], v[10:11]
	v_pk_mul_f32 v[6:7], v[6:7], v[12:13]
	v_pk_mul_f32 v[2:3], v[2:3], v[14:15]
	v_cvt_pk_bf16_f32 v3, v2, v3
	v_cvt_pk_bf16_f32 v2, v0, v1
	v_cvt_pk_bf16_f32 v0, v4, v5
	v_cvt_pk_bf16_f32 v1, v6, v7
	s_and_saveexec_b64 s[0:1], s[44:45]
	v_mul_u32_u24_e32 v4, s2, v158
	v_lshlrev_b32_e32 v5, v145, v192
	v_add3_u32 v212, v4, v5, v172
	v_lshl_add_u64 v[4:5], v[212:213], 1, s[52:53]
	global_store_dwordx4 v[4:5], v[0:3], off nt
	s_nop 1
